# speedup vs baseline: 1.0216x; 1.0177x over previous
_Z12k1_colsum_q8PKfPjPfS2_:
	s_load_dwordx8 s[4:11], s[0:1], 0x0
	v_and_b32_e32 v1, 63, v0
	v_lshrrev_b32_e32 v41, 6, v0
	s_lshl_b32 s12, s2, 3
	s_nop 0
	v_readfirstlane_b32 s14, v41
	s_add_u32 s12, s12, s14
	s_cmp_lt_u32 s12, 0x6a0
	s_cselect_b32 s29, 1, 0
	v_lshlrev_b32_e32 v34, 4, v1
	v_min_u32_e32 v35, 57, v1
	v_lshlrev_b32_e32 v35, 4, v35
	v_cmp_gt_u32_e64 s[18:19], 58, v1
	s_lshl_b32 s35, s14, 13
	s_add_u32 s36, s35, 0x1000
	v_add_u32_e32 v38, s35, v34
	v_lshrrev_b32_e32 v41, 5, v1
	v_mov_b32_e32 v42, 0xc35000
	v_mul_lo_u32 v39, v41, v42
	v_and_b32_e32 v42, 31, v1
	v_lshl_add_u32 v39, v42, 2, v39
	v_mov_b32_e32 v2, 0
	v_mov_b32_e32 v3, 0
	v_mov_b32_e32 v4, 0
	v_mov_b32_e32 v5, 0
	v_mov_b32_e32 v6, 0
	v_mov_b32_e32 v7, 0
	v_mov_b32_e32 v8, 0
	v_mov_b32_e32 v9, 0
	v_mov_b32_e32 v10, 0
	v_mov_b32_e32 v11, 0
	v_mov_b32_e32 v12, 0
	v_mov_b32_e32 v13, 0
	v_mov_b32_e32 v14, 0
	v_mov_b32_e32 v15, 0
	v_mov_b32_e32 v16, 0
	v_mov_b32_e32 v17, 0
	v_mov_b32_e32 v40, 0
	v_mov_b32_e32 v47, 0x42fe0000
	s_mov_b32 s32, 0x42fe0000
	s_mov_b32 s33, 0xc0c0400
	s_mov_b32 s34, 0x4000c0c
	s_mov_b32 s15, s12
	s_mul_i32 s37, s15, 0xfa0
	s_lshl_b32 s15, s15, 7
	s_waitcnt lgkmcnt(0)
	s_add_u32 s16, s4, s37
	s_addc_u32 s17, s5, 0
	s_add_u32 s40, s6, s15
	s_addc_u32 s41, s7, 0
	s_add_u32 s20, s40, 0
	s_addc_u32 s21, s41, 0
	s_add_u32 s22, s20, 0x186a000
	s_addc_u32 s23, s21, 0
	s_add_u32 s24, s22, 0x186a000
	s_addc_u32 s25, s23, 0
	s_add_u32 s26, s24, 0x186a000
	s_addc_u32 s27, s25, 0
	s_mov_b32 m0, s35
	s_nop 0
	global_load_lds_dwordx4 v34, s[16:17] nt
	global_load_lds_dwordx4 v34, s[16:17] offset:1024 nt
	global_load_lds_dwordx4 v34, s[16:17] offset:2048 nt
	global_load_lds_dwordx4 v35, s[16:17] offset:3072 nt
	s_add_u32 s16, s16, 0xfa0000
	s_addc_u32 s17, s17, 0
	s_waitcnt vmcnt(0)
	ds_read_b128 v[18:21], v38 offset:0
	ds_read_b128 v[22:25], v38 offset:1024
	ds_read_b128 v[26:29], v38 offset:2048
	ds_read_b128 v[30:33], v38 offset:3072
	s_waitcnt lgkmcnt(0)
	s_barrier
	s_mov_b32 m0, s36
	s_nop 0
	global_load_lds_dwordx4 v34, s[16:17] nt
	global_load_lds_dwordx4 v34, s[16:17] offset:1024 nt
	global_load_lds_dwordx4 v34, s[16:17] offset:2048 nt
	global_load_lds_dwordx4 v35, s[16:17] offset:3072 nt
	s_add_u32 s16, s16, 0xfa0000
	s_addc_u32 s17, s17, 0
	v_cndmask_b32_e64 v30, 0, v30, s[18:19]
	v_cndmask_b32_e64 v31, 0, v31, s[18:19]
	v_cndmask_b32_e64 v32, 0, v32, s[18:19]
	v_cndmask_b32_e64 v33, 0, v33, s[18:19]
	v_max3_f32 v41, |v18|, |v19|, |v20|
	v_max3_f32 v42, |v21|, |v22|, |v23|
	v_max3_f32 v43, |v24|, |v25|, |v26|
	v_max3_f32 v44, |v27|, |v28|, |v29|
	v_max3_f32 v48, |v30|, |v31|, |v32|
	v_max3_f32 v41, v41, v42, |v33|
	v_max3_f32 v43, v43, v44, v48
	v_max_f32_e32 v41, v41, v43
	v_pk_add_f32 v[2:3], v[2:3], v[18:19]
	v_pk_add_f32 v[4:5], v[4:5], v[20:21]
	v_max_f32_dpp v41, v41, v41 quad_perm:[1,0,3,2] row_mask:0xf bank_mask:0xf
	v_pk_add_f32 v[6:7], v[6:7], v[22:23]
	v_pk_add_f32 v[8:9], v[8:9], v[24:25]
	v_max_f32_dpp v41, v41, v41 quad_perm:[2,3,0,1] row_mask:0xf bank_mask:0xf
	v_pk_add_f32 v[10:11], v[10:11], v[26:27]
	v_pk_add_f32 v[12:13], v[12:13], v[28:29]
	v_max_f32_dpp v41, v41, v41 row_half_mirror row_mask:0xf bank_mask:0xf
	v_pk_add_f32 v[14:15], v[14:15], v[30:31]
	v_pk_add_f32 v[16:17], v[16:17], v[32:33]
	v_max_f32_dpp v41, v41, v41 row_mirror row_mask:0xf bank_mask:0xf
	s_nop 1
	v_max_f32_dpp v41, v41, v41 row_bcast:15 row_mask:0xa bank_mask:0xf
	s_nop 1
	v_max_f32_dpp v41, v41, v41 row_bcast:31 row_mask:0xc bank_mask:0xf
	s_nop 1
	v_readlane_b32 s28, v41, 63
	s_nop 1
	v_div_scale_f32 v48, s[30:31], s28, s28, v47
	v_rcp_f32_e32 v49, v48
	s_nop 0
	v_fma_f32 v50, -v48, v49, 1.0
	v_fmac_f32_e32 v49, v50, v49
	v_mov_b32_e32 v50, s28
	v_div_scale_f32 v50, vcc, s32, v50, s32
	v_mul_f32_e32 v51, v50, v49
	v_fma_f32 v52, -v48, v51, v50
	v_fmac_f32_e32 v51, v52, v49
	v_fma_f32 v48, -v48, v51, v50
	v_div_fmas_f32 v48, v48, v49, v51
	v_div_fixup_f32 v48, v48, s28, v47
	v_cmp_gt_f32_e64 vcc, s28, 0
	v_writelane_b32 v40, s28, 0
	s_nop 0
	v_cndmask_b32_e32 v48, 0, v48, vcc
	v_fmaak_f32 v49, v18, v48, 0x4b400000
	v_fmaak_f32 v50, v19, v48, 0x4b400000
	v_fmaak_f32 v51, v20, v48, 0x4b400000
	v_fmaak_f32 v52, v21, v48, 0x4b400000
	v_perm_b32 v49, v50, v49, s33
	v_perm_b32 v51, v52, v51, s34
	v_or_b32_e32 v56, v49, v51
	v_fmaak_f32 v41, v22, v48, 0x4b400000
	v_fmaak_f32 v42, v23, v48, 0x4b400000
	v_fmaak_f32 v43, v24, v48, 0x4b400000
	v_fmaak_f32 v44, v25, v48, 0x4b400000
	v_perm_b32 v41, v42, v41, s33
	v_perm_b32 v43, v44, v43, s34
	v_or_b32_e32 v57, v41, v43
	v_fmaak_f32 v49, v26, v48, 0x4b400000
	v_fmaak_f32 v50, v27, v48, 0x4b400000
	v_fmaak_f32 v51, v28, v48, 0x4b400000
	v_fmaak_f32 v52, v29, v48, 0x4b400000
	v_perm_b32 v49, v50, v49, s33
	v_perm_b32 v51, v52, v51, s34
	v_or_b32_e32 v58, v49, v51
	v_fmaak_f32 v41, v30, v48, 0x4b400000
	v_fmaak_f32 v42, v31, v48, 0x4b400000
	v_fmaak_f32 v43, v32, v48, 0x4b400000
	v_fmaak_f32 v44, v33, v48, 0x4b400000
	v_perm_b32 v41, v42, v41, s33
	v_perm_b32 v43, v44, v43, s34
	v_or_b32_e32 v59, v41, v43
	s_waitcnt vmcnt(0)
	ds_read_b128 v[18:21], v38 offset:4096
	ds_read_b128 v[22:25], v38 offset:5120
	ds_read_b128 v[26:29], v38 offset:6144
	ds_read_b128 v[30:33], v38 offset:7168
	s_waitcnt lgkmcnt(0)
	s_barrier
	s_mov_b32 m0, s35
	s_nop 0
	global_load_lds_dwordx4 v34, s[16:17] nt
	global_load_lds_dwordx4 v34, s[16:17] offset:1024 nt
	global_load_lds_dwordx4 v34, s[16:17] offset:2048 nt
	global_load_lds_dwordx4 v35, s[16:17] offset:3072 nt
	s_add_u32 s16, s16, 0xfa0000
	s_addc_u32 s17, s17, 0
	v_cndmask_b32_e64 v30, 0, v30, s[18:19]
	v_cndmask_b32_e64 v31, 0, v31, s[18:19]
	v_cndmask_b32_e64 v32, 0, v32, s[18:19]
	v_cndmask_b32_e64 v33, 0, v33, s[18:19]
	v_max3_f32 v41, |v18|, |v19|, |v20|
	v_max3_f32 v42, |v21|, |v22|, |v23|
	v_max3_f32 v43, |v24|, |v25|, |v26|
	v_max3_f32 v44, |v27|, |v28|, |v29|
	v_max3_f32 v48, |v30|, |v31|, |v32|
	v_max3_f32 v41, v41, v42, |v33|
	v_max3_f32 v43, v43, v44, v48
	v_max_f32_e32 v41, v41, v43
	v_pk_add_f32 v[2:3], v[2:3], v[18:19]
	v_pk_add_f32 v[4:5], v[4:5], v[20:21]
	v_max_f32_dpp v41, v41, v41 quad_perm:[1,0,3,2] row_mask:0xf bank_mask:0xf
	v_pk_add_f32 v[6:7], v[6:7], v[22:23]
	v_pk_add_f32 v[8:9], v[8:9], v[24:25]
	v_max_f32_dpp v41, v41, v41 quad_perm:[2,3,0,1] row_mask:0xf bank_mask:0xf
	v_pk_add_f32 v[10:11], v[10:11], v[26:27]
	v_pk_add_f32 v[12:13], v[12:13], v[28:29]
	v_max_f32_dpp v41, v41, v41 row_half_mirror row_mask:0xf bank_mask:0xf
	v_pk_add_f32 v[14:15], v[14:15], v[30:31]
	v_pk_add_f32 v[16:17], v[16:17], v[32:33]
	v_max_f32_dpp v41, v41, v41 row_mirror row_mask:0xf bank_mask:0xf
	s_nop 1
	v_max_f32_dpp v41, v41, v41 row_bcast:15 row_mask:0xa bank_mask:0xf
	s_nop 1
	v_max_f32_dpp v41, v41, v41 row_bcast:31 row_mask:0xc bank_mask:0xf
	s_nop 1
	v_readlane_b32 s28, v41, 63
	s_nop 1
	v_div_scale_f32 v48, s[30:31], s28, s28, v47
	v_rcp_f32_e32 v49, v48
	s_nop 0
	v_fma_f32 v50, -v48, v49, 1.0
	v_fmac_f32_e32 v49, v50, v49
	v_mov_b32_e32 v50, s28
	v_div_scale_f32 v50, vcc, s32, v50, s32
	v_mul_f32_e32 v51, v50, v49
	v_fma_f32 v52, -v48, v51, v50
	v_fmac_f32_e32 v51, v52, v49
	v_fma_f32 v48, -v48, v51, v50
	v_div_fmas_f32 v48, v48, v49, v51
	v_div_fixup_f32 v48, v48, s28, v47
	v_cmp_gt_f32_e64 vcc, s28, 0
	v_writelane_b32 v40, s28, 1
	s_nop 0
	v_cndmask_b32_e32 v48, 0, v48, vcc
	v_fmaak_f32 v49, v18, v48, 0x4b400000
	v_fmaak_f32 v50, v19, v48, 0x4b400000
	v_fmaak_f32 v51, v20, v48, 0x4b400000
	v_fmaak_f32 v52, v21, v48, 0x4b400000
	v_perm_b32 v49, v50, v49, s33
	v_perm_b32 v51, v52, v51, s34
	v_or_b32_e32 v60, v49, v51
	v_fmaak_f32 v41, v22, v48, 0x4b400000
	v_fmaak_f32 v42, v23, v48, 0x4b400000
	v_fmaak_f32 v43, v24, v48, 0x4b400000
	v_fmaak_f32 v44, v25, v48, 0x4b400000
	v_perm_b32 v41, v42, v41, s33
	v_perm_b32 v43, v44, v43, s34
	v_or_b32_e32 v61, v41, v43
	v_fmaak_f32 v49, v26, v48, 0x4b400000
	v_fmaak_f32 v50, v27, v48, 0x4b400000
	v_fmaak_f32 v51, v28, v48, 0x4b400000
	v_fmaak_f32 v52, v29, v48, 0x4b400000
	v_perm_b32 v49, v50, v49, s33
	v_perm_b32 v51, v52, v51, s34
	v_or_b32_e32 v62, v49, v51
	v_fmaak_f32 v41, v30, v48, 0x4b400000
	v_fmaak_f32 v42, v31, v48, 0x4b400000
	v_fmaak_f32 v43, v32, v48, 0x4b400000
	v_fmaak_f32 v44, v33, v48, 0x4b400000
	v_perm_b32 v41, v42, v41, s33
	v_perm_b32 v43, v44, v43, s34
	v_or_b32_e32 v63, v41, v43
	s_waitcnt vmcnt(0)
	ds_read_b128 v[18:21], v38 offset:0
	ds_read_b128 v[22:25], v38 offset:1024
	ds_read_b128 v[26:29], v38 offset:2048
	ds_read_b128 v[30:33], v38 offset:3072
	s_waitcnt lgkmcnt(0)
	s_barrier
	s_mov_b32 m0, s36
	s_nop 0
	global_load_lds_dwordx4 v34, s[16:17] nt
	global_load_lds_dwordx4 v34, s[16:17] offset:1024 nt
	global_load_lds_dwordx4 v34, s[16:17] offset:2048 nt
	global_load_lds_dwordx4 v35, s[16:17] offset:3072 nt
	s_add_u32 s16, s16, 0xfa0000
	s_addc_u32 s17, s17, 0
	v_cndmask_b32_e64 v30, 0, v30, s[18:19]
	v_cndmask_b32_e64 v31, 0, v31, s[18:19]
	v_cndmask_b32_e64 v32, 0, v32, s[18:19]
	v_cndmask_b32_e64 v33, 0, v33, s[18:19]
	v_max3_f32 v41, |v18|, |v19|, |v20|
	v_max3_f32 v42, |v21|, |v22|, |v23|
	v_max3_f32 v43, |v24|, |v25|, |v26|
	v_max3_f32 v44, |v27|, |v28|, |v29|
	v_max3_f32 v48, |v30|, |v31|, |v32|
	v_max3_f32 v41, v41, v42, |v33|
	v_max3_f32 v43, v43, v44, v48
	v_max_f32_e32 v41, v41, v43
	v_pk_add_f32 v[2:3], v[2:3], v[18:19]
	v_pk_add_f32 v[4:5], v[4:5], v[20:21]
	v_max_f32_dpp v41, v41, v41 quad_perm:[1,0,3,2] row_mask:0xf bank_mask:0xf
	v_pk_add_f32 v[6:7], v[6:7], v[22:23]
	v_pk_add_f32 v[8:9], v[8:9], v[24:25]
	v_max_f32_dpp v41, v41, v41 quad_perm:[2,3,0,1] row_mask:0xf bank_mask:0xf
	v_pk_add_f32 v[10:11], v[10:11], v[26:27]
	v_pk_add_f32 v[12:13], v[12:13], v[28:29]
	v_max_f32_dpp v41, v41, v41 row_half_mirror row_mask:0xf bank_mask:0xf
	v_pk_add_f32 v[14:15], v[14:15], v[30:31]
	v_pk_add_f32 v[16:17], v[16:17], v[32:33]
	v_max_f32_dpp v41, v41, v41 row_mirror row_mask:0xf bank_mask:0xf
	s_nop 1
	v_max_f32_dpp v41, v41, v41 row_bcast:15 row_mask:0xa bank_mask:0xf
	s_nop 1
	v_max_f32_dpp v41, v41, v41 row_bcast:31 row_mask:0xc bank_mask:0xf
	s_nop 1
	v_readlane_b32 s28, v41, 63
	s_nop 1
	v_div_scale_f32 v48, s[30:31], s28, s28, v47
	v_rcp_f32_e32 v49, v48
	s_nop 0
	v_fma_f32 v50, -v48, v49, 1.0
	v_fmac_f32_e32 v49, v50, v49
	v_mov_b32_e32 v50, s28
	v_div_scale_f32 v50, vcc, s32, v50, s32
	v_mul_f32_e32 v51, v50, v49
	v_fma_f32 v52, -v48, v51, v50
	v_fmac_f32_e32 v51, v52, v49
	v_fma_f32 v48, -v48, v51, v50
	v_div_fmas_f32 v48, v48, v49, v51
	v_div_fixup_f32 v48, v48, s28, v47
	v_cmp_gt_f32_e64 vcc, s28, 0
	v_writelane_b32 v40, s28, 2
	s_nop 0
	v_cndmask_b32_e32 v48, 0, v48, vcc
	v_fmaak_f32 v49, v18, v48, 0x4b400000
	v_fmaak_f32 v50, v19, v48, 0x4b400000
	v_fmaak_f32 v51, v20, v48, 0x4b400000
	v_fmaak_f32 v52, v21, v48, 0x4b400000
	v_perm_b32 v49, v50, v49, s33
	v_perm_b32 v51, v52, v51, s34
	v_or_b32_e32 v64, v49, v51
	v_fmaak_f32 v41, v22, v48, 0x4b400000
	v_fmaak_f32 v42, v23, v48, 0x4b400000
	v_fmaak_f32 v43, v24, v48, 0x4b400000
	v_fmaak_f32 v44, v25, v48, 0x4b400000
	v_perm_b32 v41, v42, v41, s33
	v_perm_b32 v43, v44, v43, s34
	v_or_b32_e32 v65, v41, v43
	v_fmaak_f32 v49, v26, v48, 0x4b400000
	v_fmaak_f32 v50, v27, v48, 0x4b400000
	v_fmaak_f32 v51, v28, v48, 0x4b400000
	v_fmaak_f32 v52, v29, v48, 0x4b400000
	v_perm_b32 v49, v50, v49, s33
	v_perm_b32 v51, v52, v51, s34
	v_or_b32_e32 v66, v49, v51
	v_fmaak_f32 v41, v30, v48, 0x4b400000
	v_fmaak_f32 v42, v31, v48, 0x4b400000
	v_fmaak_f32 v43, v32, v48, 0x4b400000
	v_fmaak_f32 v44, v33, v48, 0x4b400000
	v_perm_b32 v41, v42, v41, s33
	v_perm_b32 v43, v44, v43, s34
	v_or_b32_e32 v67, v41, v43
	s_waitcnt vmcnt(0)
	ds_read_b128 v[18:21], v38 offset:4096
	ds_read_b128 v[22:25], v38 offset:5120
	ds_read_b128 v[26:29], v38 offset:6144
	ds_read_b128 v[30:33], v38 offset:7168
	s_waitcnt lgkmcnt(0)
	s_barrier
	s_mov_b32 m0, s35
	s_nop 0
	global_load_lds_dwordx4 v34, s[16:17] nt
	global_load_lds_dwordx4 v34, s[16:17] offset:1024 nt
	global_load_lds_dwordx4 v34, s[16:17] offset:2048 nt
	global_load_lds_dwordx4 v35, s[16:17] offset:3072 nt
	s_add_u32 s16, s16, 0xfa0000
	s_addc_u32 s17, s17, 0
	v_cndmask_b32_e64 v30, 0, v30, s[18:19]
	v_cndmask_b32_e64 v31, 0, v31, s[18:19]
	v_cndmask_b32_e64 v32, 0, v32, s[18:19]
	v_cndmask_b32_e64 v33, 0, v33, s[18:19]
	v_max3_f32 v41, |v18|, |v19|, |v20|
	v_max3_f32 v42, |v21|, |v22|, |v23|
	v_max3_f32 v43, |v24|, |v25|, |v26|
	v_max3_f32 v44, |v27|, |v28|, |v29|
	v_max3_f32 v48, |v30|, |v31|, |v32|
	v_max3_f32 v41, v41, v42, |v33|
	v_max3_f32 v43, v43, v44, v48
	v_max_f32_e32 v41, v41, v43
	v_pk_add_f32 v[2:3], v[2:3], v[18:19]
	v_pk_add_f32 v[4:5], v[4:5], v[20:21]
	v_max_f32_dpp v41, v41, v41 quad_perm:[1,0,3,2] row_mask:0xf bank_mask:0xf
	v_pk_add_f32 v[6:7], v[6:7], v[22:23]
	v_pk_add_f32 v[8:9], v[8:9], v[24:25]
	v_max_f32_dpp v41, v41, v41 quad_perm:[2,3,0,1] row_mask:0xf bank_mask:0xf
	v_pk_add_f32 v[10:11], v[10:11], v[26:27]
	v_pk_add_f32 v[12:13], v[12:13], v[28:29]
	v_max_f32_dpp v41, v41, v41 row_half_mirror row_mask:0xf bank_mask:0xf
	v_pk_add_f32 v[14:15], v[14:15], v[30:31]
	v_pk_add_f32 v[16:17], v[16:17], v[32:33]
	v_max_f32_dpp v41, v41, v41 row_mirror row_mask:0xf bank_mask:0xf
	s_nop 1
	v_max_f32_dpp v41, v41, v41 row_bcast:15 row_mask:0xa bank_mask:0xf
	s_nop 1
	v_max_f32_dpp v41, v41, v41 row_bcast:31 row_mask:0xc bank_mask:0xf
	s_nop 1
	v_readlane_b32 s28, v41, 63
	s_nop 1
	v_div_scale_f32 v48, s[30:31], s28, s28, v47
	v_rcp_f32_e32 v49, v48
	s_nop 0
	v_fma_f32 v50, -v48, v49, 1.0
	v_fmac_f32_e32 v49, v50, v49
	v_mov_b32_e32 v50, s28
	v_div_scale_f32 v50, vcc, s32, v50, s32
	v_mul_f32_e32 v51, v50, v49
	v_fma_f32 v52, -v48, v51, v50
	v_fmac_f32_e32 v51, v52, v49
	v_fma_f32 v48, -v48, v51, v50
	v_div_fmas_f32 v48, v48, v49, v51
	v_div_fixup_f32 v48, v48, s28, v47
	v_cmp_gt_f32_e64 vcc, s28, 0
	v_writelane_b32 v40, s28, 3
	s_nop 0
	v_cndmask_b32_e32 v48, 0, v48, vcc
	v_fmaak_f32 v49, v18, v48, 0x4b400000
	v_fmaak_f32 v50, v19, v48, 0x4b400000
	v_fmaak_f32 v51, v20, v48, 0x4b400000
	v_fmaak_f32 v52, v21, v48, 0x4b400000
	v_perm_b32 v49, v50, v49, s33
	v_perm_b32 v51, v52, v51, s34
	v_or_b32_e32 v68, v49, v51
	v_fmaak_f32 v41, v22, v48, 0x4b400000
	v_fmaak_f32 v42, v23, v48, 0x4b400000
	v_fmaak_f32 v43, v24, v48, 0x4b400000
	v_fmaak_f32 v44, v25, v48, 0x4b400000
	v_perm_b32 v41, v42, v41, s33
	v_perm_b32 v43, v44, v43, s34
	v_or_b32_e32 v69, v41, v43
	v_fmaak_f32 v49, v26, v48, 0x4b400000
	v_fmaak_f32 v50, v27, v48, 0x4b400000
	v_fmaak_f32 v51, v28, v48, 0x4b400000
	v_fmaak_f32 v52, v29, v48, 0x4b400000
	v_perm_b32 v49, v50, v49, s33
	v_perm_b32 v51, v52, v51, s34
	v_or_b32_e32 v70, v49, v51
	v_fmaak_f32 v41, v30, v48, 0x4b400000
	v_fmaak_f32 v42, v31, v48, 0x4b400000
	v_fmaak_f32 v43, v32, v48, 0x4b400000
	v_fmaak_f32 v44, v33, v48, 0x4b400000
	v_perm_b32 v41, v42, v41, s33
	v_perm_b32 v43, v44, v43, s34
	v_or_b32_e32 v71, v41, v43
	s_waitcnt vmcnt(0)
	ds_read_b128 v[18:21], v38 offset:0
	ds_read_b128 v[22:25], v38 offset:1024
	ds_read_b128 v[26:29], v38 offset:2048
	ds_read_b128 v[30:33], v38 offset:3072
	s_waitcnt lgkmcnt(0)
	s_barrier
	s_mov_b32 m0, s36
	s_nop 0
	global_load_lds_dwordx4 v34, s[16:17] nt
	global_load_lds_dwordx4 v34, s[16:17] offset:1024 nt
	global_load_lds_dwordx4 v34, s[16:17] offset:2048 nt
	global_load_lds_dwordx4 v35, s[16:17] offset:3072 nt
	s_add_u32 s16, s16, 0xfa0000
	s_addc_u32 s17, s17, 0
	v_cndmask_b32_e64 v30, 0, v30, s[18:19]
	v_cndmask_b32_e64 v31, 0, v31, s[18:19]
	v_cndmask_b32_e64 v32, 0, v32, s[18:19]
	v_cndmask_b32_e64 v33, 0, v33, s[18:19]
	v_max3_f32 v41, |v18|, |v19|, |v20|
	v_max3_f32 v42, |v21|, |v22|, |v23|
	v_max3_f32 v43, |v24|, |v25|, |v26|
	v_max3_f32 v44, |v27|, |v28|, |v29|
	v_max3_f32 v48, |v30|, |v31|, |v32|
	v_max3_f32 v41, v41, v42, |v33|
	v_max3_f32 v43, v43, v44, v48
	v_max_f32_e32 v41, v41, v43
	v_pk_add_f32 v[2:3], v[2:3], v[18:19]
	v_pk_add_f32 v[4:5], v[4:5], v[20:21]
	v_max_f32_dpp v41, v41, v41 quad_perm:[1,0,3,2] row_mask:0xf bank_mask:0xf
	v_pk_add_f32 v[6:7], v[6:7], v[22:23]
	v_pk_add_f32 v[8:9], v[8:9], v[24:25]
	v_max_f32_dpp v41, v41, v41 quad_perm:[2,3,0,1] row_mask:0xf bank_mask:0xf
	v_pk_add_f32 v[10:11], v[10:11], v[26:27]
	v_pk_add_f32 v[12:13], v[12:13], v[28:29]
	v_max_f32_dpp v41, v41, v41 row_half_mirror row_mask:0xf bank_mask:0xf
	v_pk_add_f32 v[14:15], v[14:15], v[30:31]
	v_pk_add_f32 v[16:17], v[16:17], v[32:33]
	v_max_f32_dpp v41, v41, v41 row_mirror row_mask:0xf bank_mask:0xf
	s_nop 1
	v_max_f32_dpp v41, v41, v41 row_bcast:15 row_mask:0xa bank_mask:0xf
	s_nop 1
	v_max_f32_dpp v41, v41, v41 row_bcast:31 row_mask:0xc bank_mask:0xf
	s_nop 1
	v_readlane_b32 s28, v41, 63
	s_nop 1
	v_div_scale_f32 v48, s[30:31], s28, s28, v47
	v_rcp_f32_e32 v49, v48
	s_nop 0
	v_fma_f32 v50, -v48, v49, 1.0
	v_fmac_f32_e32 v49, v50, v49
	v_mov_b32_e32 v50, s28
	v_div_scale_f32 v50, vcc, s32, v50, s32
	v_mul_f32_e32 v51, v50, v49
	v_fma_f32 v52, -v48, v51, v50
	v_fmac_f32_e32 v51, v52, v49
	v_fma_f32 v48, -v48, v51, v50
	v_div_fmas_f32 v48, v48, v49, v51
	v_div_fixup_f32 v48, v48, s28, v47
	v_cmp_gt_f32_e64 vcc, s28, 0
	v_writelane_b32 v40, s28, 4
	s_nop 0
	v_cndmask_b32_e32 v48, 0, v48, vcc
	v_fmaak_f32 v49, v18, v48, 0x4b400000
	v_fmaak_f32 v50, v19, v48, 0x4b400000
	v_fmaak_f32 v51, v20, v48, 0x4b400000
	v_fmaak_f32 v52, v21, v48, 0x4b400000
	v_perm_b32 v49, v50, v49, s33
	v_perm_b32 v51, v52, v51, s34
	v_or_b32_e32 v72, v49, v51
	v_fmaak_f32 v41, v22, v48, 0x4b400000
	v_fmaak_f32 v42, v23, v48, 0x4b400000
	v_fmaak_f32 v43, v24, v48, 0x4b400000
	v_fmaak_f32 v44, v25, v48, 0x4b400000
	v_perm_b32 v41, v42, v41, s33
	v_perm_b32 v43, v44, v43, s34
	v_or_b32_e32 v73, v41, v43
	v_fmaak_f32 v49, v26, v48, 0x4b400000
	v_fmaak_f32 v50, v27, v48, 0x4b400000
	v_fmaak_f32 v51, v28, v48, 0x4b400000
	v_fmaak_f32 v52, v29, v48, 0x4b400000
	v_perm_b32 v49, v50, v49, s33
	v_perm_b32 v51, v52, v51, s34
	v_or_b32_e32 v74, v49, v51
	v_fmaak_f32 v41, v30, v48, 0x4b400000
	v_fmaak_f32 v42, v31, v48, 0x4b400000
	v_fmaak_f32 v43, v32, v48, 0x4b400000
	v_fmaak_f32 v44, v33, v48, 0x4b400000
	v_perm_b32 v41, v42, v41, s33
	v_perm_b32 v43, v44, v43, s34
	v_or_b32_e32 v75, v41, v43
	s_waitcnt vmcnt(0)
	ds_read_b128 v[18:21], v38 offset:4096
	ds_read_b128 v[22:25], v38 offset:5120
	ds_read_b128 v[26:29], v38 offset:6144
	ds_read_b128 v[30:33], v38 offset:7168
	s_waitcnt lgkmcnt(0)
	s_barrier
	s_mov_b32 m0, s35
	s_nop 0
	global_load_lds_dwordx4 v34, s[16:17] nt
	global_load_lds_dwordx4 v34, s[16:17] offset:1024 nt
	global_load_lds_dwordx4 v34, s[16:17] offset:2048 nt
	global_load_lds_dwordx4 v35, s[16:17] offset:3072 nt
	s_add_u32 s16, s16, 0xfa0000
	s_addc_u32 s17, s17, 0
	v_cndmask_b32_e64 v30, 0, v30, s[18:19]
	v_cndmask_b32_e64 v31, 0, v31, s[18:19]
	v_cndmask_b32_e64 v32, 0, v32, s[18:19]
	v_cndmask_b32_e64 v33, 0, v33, s[18:19]
	v_max3_f32 v41, |v18|, |v19|, |v20|
	v_max3_f32 v42, |v21|, |v22|, |v23|
	v_max3_f32 v43, |v24|, |v25|, |v26|
	v_max3_f32 v44, |v27|, |v28|, |v29|
	v_max3_f32 v48, |v30|, |v31|, |v32|
	v_max3_f32 v41, v41, v42, |v33|
	v_max3_f32 v43, v43, v44, v48
	v_max_f32_e32 v41, v41, v43
	v_pk_add_f32 v[2:3], v[2:3], v[18:19]
	v_pk_add_f32 v[4:5], v[4:5], v[20:21]
	v_max_f32_dpp v41, v41, v41 quad_perm:[1,0,3,2] row_mask:0xf bank_mask:0xf
	v_pk_add_f32 v[6:7], v[6:7], v[22:23]
	v_pk_add_f32 v[8:9], v[8:9], v[24:25]
	v_max_f32_dpp v41, v41, v41 quad_perm:[2,3,0,1] row_mask:0xf bank_mask:0xf
	v_pk_add_f32 v[10:11], v[10:11], v[26:27]
	v_pk_add_f32 v[12:13], v[12:13], v[28:29]
	v_max_f32_dpp v41, v41, v41 row_half_mirror row_mask:0xf bank_mask:0xf
	v_pk_add_f32 v[14:15], v[14:15], v[30:31]
	v_pk_add_f32 v[16:17], v[16:17], v[32:33]
	v_max_f32_dpp v41, v41, v41 row_mirror row_mask:0xf bank_mask:0xf
	s_nop 1
	v_max_f32_dpp v41, v41, v41 row_bcast:15 row_mask:0xa bank_mask:0xf
	s_nop 1
	v_max_f32_dpp v41, v41, v41 row_bcast:31 row_mask:0xc bank_mask:0xf
	s_nop 1
	v_readlane_b32 s28, v41, 63
	s_nop 1
	v_div_scale_f32 v48, s[30:31], s28, s28, v47
	v_rcp_f32_e32 v49, v48
	s_nop 0
	v_fma_f32 v50, -v48, v49, 1.0
	v_fmac_f32_e32 v49, v50, v49
	v_mov_b32_e32 v50, s28
	v_div_scale_f32 v50, vcc, s32, v50, s32
	v_mul_f32_e32 v51, v50, v49
	v_fma_f32 v52, -v48, v51, v50
	v_fmac_f32_e32 v51, v52, v49
	v_fma_f32 v48, -v48, v51, v50
	v_div_fmas_f32 v48, v48, v49, v51
	v_div_fixup_f32 v48, v48, s28, v47
	v_cmp_gt_f32_e64 vcc, s28, 0
	v_writelane_b32 v40, s28, 5
	s_nop 0
	v_cndmask_b32_e32 v48, 0, v48, vcc
	v_fmaak_f32 v49, v18, v48, 0x4b400000
	v_fmaak_f32 v50, v19, v48, 0x4b400000
	v_fmaak_f32 v51, v20, v48, 0x4b400000
	v_fmaak_f32 v52, v21, v48, 0x4b400000
	v_perm_b32 v49, v50, v49, s33
	v_perm_b32 v51, v52, v51, s34
	v_or_b32_e32 v76, v49, v51
	v_fmaak_f32 v41, v22, v48, 0x4b400000
	v_fmaak_f32 v42, v23, v48, 0x4b400000
	v_fmaak_f32 v43, v24, v48, 0x4b400000
	v_fmaak_f32 v44, v25, v48, 0x4b400000
	v_perm_b32 v41, v42, v41, s33
	v_perm_b32 v43, v44, v43, s34
	v_or_b32_e32 v77, v41, v43
	v_fmaak_f32 v49, v26, v48, 0x4b400000
	v_fmaak_f32 v50, v27, v48, 0x4b400000
	v_fmaak_f32 v51, v28, v48, 0x4b400000
	v_fmaak_f32 v52, v29, v48, 0x4b400000
	v_perm_b32 v49, v50, v49, s33
	v_perm_b32 v51, v52, v51, s34
	v_or_b32_e32 v78, v49, v51
	v_fmaak_f32 v41, v30, v48, 0x4b400000
	v_fmaak_f32 v42, v31, v48, 0x4b400000
	v_fmaak_f32 v43, v32, v48, 0x4b400000
	v_fmaak_f32 v44, v33, v48, 0x4b400000
	v_perm_b32 v41, v42, v41, s33
	v_perm_b32 v43, v44, v43, s34
	v_or_b32_e32 v79, v41, v43
	s_waitcnt vmcnt(0)
	ds_read_b128 v[18:21], v38 offset:0
	ds_read_b128 v[22:25], v38 offset:1024
	ds_read_b128 v[26:29], v38 offset:2048
	ds_read_b128 v[30:33], v38 offset:3072
	s_waitcnt lgkmcnt(0)
	s_barrier
	s_mov_b32 m0, s36
	s_nop 0
	global_load_lds_dwordx4 v34, s[16:17] nt
	global_load_lds_dwordx4 v34, s[16:17] offset:1024 nt
	global_load_lds_dwordx4 v34, s[16:17] offset:2048 nt
	global_load_lds_dwordx4 v35, s[16:17] offset:3072 nt
	s_add_u32 s16, s16, 0xfa0000
	s_addc_u32 s17, s17, 0
	v_cndmask_b32_e64 v30, 0, v30, s[18:19]
	v_cndmask_b32_e64 v31, 0, v31, s[18:19]
	v_cndmask_b32_e64 v32, 0, v32, s[18:19]
	v_cndmask_b32_e64 v33, 0, v33, s[18:19]
	v_max3_f32 v41, |v18|, |v19|, |v20|
	v_max3_f32 v42, |v21|, |v22|, |v23|
	v_max3_f32 v43, |v24|, |v25|, |v26|
	v_max3_f32 v44, |v27|, |v28|, |v29|
	v_max3_f32 v48, |v30|, |v31|, |v32|
	v_max3_f32 v41, v41, v42, |v33|
	v_max3_f32 v43, v43, v44, v48
	v_max_f32_e32 v41, v41, v43
	v_pk_add_f32 v[2:3], v[2:3], v[18:19]
	v_pk_add_f32 v[4:5], v[4:5], v[20:21]
	v_max_f32_dpp v41, v41, v41 quad_perm:[1,0,3,2] row_mask:0xf bank_mask:0xf
	v_pk_add_f32 v[6:7], v[6:7], v[22:23]
	v_pk_add_f32 v[8:9], v[8:9], v[24:25]
	v_max_f32_dpp v41, v41, v41 quad_perm:[2,3,0,1] row_mask:0xf bank_mask:0xf
	v_pk_add_f32 v[10:11], v[10:11], v[26:27]
	v_pk_add_f32 v[12:13], v[12:13], v[28:29]
	v_max_f32_dpp v41, v41, v41 row_half_mirror row_mask:0xf bank_mask:0xf
	v_pk_add_f32 v[14:15], v[14:15], v[30:31]
	v_pk_add_f32 v[16:17], v[16:17], v[32:33]
	v_max_f32_dpp v41, v41, v41 row_mirror row_mask:0xf bank_mask:0xf
	s_nop 1
	v_max_f32_dpp v41, v41, v41 row_bcast:15 row_mask:0xa bank_mask:0xf
	s_nop 1
	v_max_f32_dpp v41, v41, v41 row_bcast:31 row_mask:0xc bank_mask:0xf
	s_nop 1
	v_readlane_b32 s28, v41, 63
	s_nop 1
	v_div_scale_f32 v48, s[30:31], s28, s28, v47
	v_rcp_f32_e32 v49, v48
	s_nop 0
	v_fma_f32 v50, -v48, v49, 1.0
	v_fmac_f32_e32 v49, v50, v49
	v_mov_b32_e32 v50, s28
	v_div_scale_f32 v50, vcc, s32, v50, s32
	v_mul_f32_e32 v51, v50, v49
	v_fma_f32 v52, -v48, v51, v50
	v_fmac_f32_e32 v51, v52, v49
	v_fma_f32 v48, -v48, v51, v50
	v_div_fmas_f32 v48, v48, v49, v51
	v_div_fixup_f32 v48, v48, s28, v47
	v_cmp_gt_f32_e64 vcc, s28, 0
	v_writelane_b32 v40, s28, 6
	s_nop 0
	v_cndmask_b32_e32 v48, 0, v48, vcc
	v_fmaak_f32 v49, v18, v48, 0x4b400000
	v_fmaak_f32 v50, v19, v48, 0x4b400000
	v_fmaak_f32 v51, v20, v48, 0x4b400000
	v_fmaak_f32 v52, v21, v48, 0x4b400000
	v_perm_b32 v49, v50, v49, s33
	v_perm_b32 v51, v52, v51, s34
	v_or_b32_e32 v80, v49, v51
	v_fmaak_f32 v41, v22, v48, 0x4b400000
	v_fmaak_f32 v42, v23, v48, 0x4b400000
	v_fmaak_f32 v43, v24, v48, 0x4b400000
	v_fmaak_f32 v44, v25, v48, 0x4b400000
	v_perm_b32 v41, v42, v41, s33
	v_perm_b32 v43, v44, v43, s34
	v_or_b32_e32 v81, v41, v43
	v_fmaak_f32 v49, v26, v48, 0x4b400000
	v_fmaak_f32 v50, v27, v48, 0x4b400000
	v_fmaak_f32 v51, v28, v48, 0x4b400000
	v_fmaak_f32 v52, v29, v48, 0x4b400000
	v_perm_b32 v49, v50, v49, s33
	v_perm_b32 v51, v52, v51, s34
	v_or_b32_e32 v82, v49, v51
	v_fmaak_f32 v41, v30, v48, 0x4b400000
	v_fmaak_f32 v42, v31, v48, 0x4b400000
	v_fmaak_f32 v43, v32, v48, 0x4b400000
	v_fmaak_f32 v44, v33, v48, 0x4b400000
	v_perm_b32 v41, v42, v41, s33
	v_perm_b32 v43, v44, v43, s34
	v_or_b32_e32 v83, v41, v43
	s_waitcnt vmcnt(0)
	ds_read_b128 v[18:21], v38 offset:4096
	ds_read_b128 v[22:25], v38 offset:5120
	ds_read_b128 v[26:29], v38 offset:6144
	ds_read_b128 v[30:33], v38 offset:7168
	s_waitcnt lgkmcnt(0)
	s_barrier
	s_mov_b32 m0, s35
	s_nop 0
	global_load_lds_dwordx4 v34, s[16:17] nt
	global_load_lds_dwordx4 v34, s[16:17] offset:1024 nt
	global_load_lds_dwordx4 v34, s[16:17] offset:2048 nt
	global_load_lds_dwordx4 v35, s[16:17] offset:3072 nt
	s_add_u32 s16, s16, 0xfa0000
	s_addc_u32 s17, s17, 0
	v_cndmask_b32_e64 v30, 0, v30, s[18:19]
	v_cndmask_b32_e64 v31, 0, v31, s[18:19]
	v_cndmask_b32_e64 v32, 0, v32, s[18:19]
	v_cndmask_b32_e64 v33, 0, v33, s[18:19]
	v_max3_f32 v41, |v18|, |v19|, |v20|
	v_max3_f32 v42, |v21|, |v22|, |v23|
	v_max3_f32 v43, |v24|, |v25|, |v26|
	v_max3_f32 v44, |v27|, |v28|, |v29|
	v_max3_f32 v48, |v30|, |v31|, |v32|
	v_max3_f32 v41, v41, v42, |v33|
	v_max3_f32 v43, v43, v44, v48
	v_max_f32_e32 v41, v41, v43
	v_pk_add_f32 v[2:3], v[2:3], v[18:19]
	v_pk_add_f32 v[4:5], v[4:5], v[20:21]
	v_max_f32_dpp v41, v41, v41 quad_perm:[1,0,3,2] row_mask:0xf bank_mask:0xf
	v_pk_add_f32 v[6:7], v[6:7], v[22:23]
	v_pk_add_f32 v[8:9], v[8:9], v[24:25]
	v_max_f32_dpp v41, v41, v41 quad_perm:[2,3,0,1] row_mask:0xf bank_mask:0xf
	v_pk_add_f32 v[10:11], v[10:11], v[26:27]
	v_pk_add_f32 v[12:13], v[12:13], v[28:29]
	v_max_f32_dpp v41, v41, v41 row_half_mirror row_mask:0xf bank_mask:0xf
	v_pk_add_f32 v[14:15], v[14:15], v[30:31]
	v_pk_add_f32 v[16:17], v[16:17], v[32:33]
	v_max_f32_dpp v41, v41, v41 row_mirror row_mask:0xf bank_mask:0xf
	s_nop 1
	v_max_f32_dpp v41, v41, v41 row_bcast:15 row_mask:0xa bank_mask:0xf
	s_nop 1
	v_max_f32_dpp v41, v41, v41 row_bcast:31 row_mask:0xc bank_mask:0xf
	s_nop 1
	v_readlane_b32 s28, v41, 63
	s_nop 1
	v_div_scale_f32 v48, s[30:31], s28, s28, v47
	v_rcp_f32_e32 v49, v48
	s_nop 0
	v_fma_f32 v50, -v48, v49, 1.0
	v_fmac_f32_e32 v49, v50, v49
	v_mov_b32_e32 v50, s28
	v_div_scale_f32 v50, vcc, s32, v50, s32
	v_mul_f32_e32 v51, v50, v49
	v_fma_f32 v52, -v48, v51, v50
	v_fmac_f32_e32 v51, v52, v49
	v_fma_f32 v48, -v48, v51, v50
	v_div_fmas_f32 v48, v48, v49, v51
	v_div_fixup_f32 v48, v48, s28, v47
	v_cmp_gt_f32_e64 vcc, s28, 0
	v_writelane_b32 v40, s28, 7
	s_nop 0
	v_cndmask_b32_e32 v48, 0, v48, vcc
	v_fmaak_f32 v49, v18, v48, 0x4b400000
	v_fmaak_f32 v50, v19, v48, 0x4b400000
	v_fmaak_f32 v51, v20, v48, 0x4b400000
	v_fmaak_f32 v52, v21, v48, 0x4b400000
	v_perm_b32 v49, v50, v49, s33
	v_perm_b32 v51, v52, v51, s34
	v_or_b32_e32 v84, v49, v51
	v_fmaak_f32 v41, v22, v48, 0x4b400000
	v_fmaak_f32 v42, v23, v48, 0x4b400000
	v_fmaak_f32 v43, v24, v48, 0x4b400000
	v_fmaak_f32 v44, v25, v48, 0x4b400000
	v_perm_b32 v41, v42, v41, s33
	v_perm_b32 v43, v44, v43, s34
	v_or_b32_e32 v85, v41, v43
	v_fmaak_f32 v49, v26, v48, 0x4b400000
	v_fmaak_f32 v50, v27, v48, 0x4b400000
	v_fmaak_f32 v51, v28, v48, 0x4b400000
	v_fmaak_f32 v52, v29, v48, 0x4b400000
	v_perm_b32 v49, v50, v49, s33
	v_perm_b32 v51, v52, v51, s34
	v_or_b32_e32 v86, v49, v51
	v_fmaak_f32 v41, v30, v48, 0x4b400000
	v_fmaak_f32 v42, v31, v48, 0x4b400000
	v_fmaak_f32 v43, v32, v48, 0x4b400000
	v_fmaak_f32 v44, v33, v48, 0x4b400000
	v_perm_b32 v41, v42, v41, s33
	v_perm_b32 v43, v44, v43, s34
	v_or_b32_e32 v87, v41, v43
	s_waitcnt vmcnt(0)
	ds_read_b128 v[18:21], v38 offset:0
	ds_read_b128 v[22:25], v38 offset:1024
	ds_read_b128 v[26:29], v38 offset:2048
	ds_read_b128 v[30:33], v38 offset:3072
	s_waitcnt lgkmcnt(0)
	s_barrier
	s_mov_b32 m0, s36
	s_nop 0
	global_load_lds_dwordx4 v34, s[16:17] nt
	global_load_lds_dwordx4 v34, s[16:17] offset:1024 nt
	global_load_lds_dwordx4 v34, s[16:17] offset:2048 nt
	global_load_lds_dwordx4 v35, s[16:17] offset:3072 nt
	s_add_u32 s16, s16, 0xfa0000
	s_addc_u32 s17, s17, 0
	v_cndmask_b32_e64 v30, 0, v30, s[18:19]
	v_cndmask_b32_e64 v31, 0, v31, s[18:19]
	v_cndmask_b32_e64 v32, 0, v32, s[18:19]
	v_cndmask_b32_e64 v33, 0, v33, s[18:19]
	v_max3_f32 v41, |v18|, |v19|, |v20|
	v_max3_f32 v42, |v21|, |v22|, |v23|
	v_max3_f32 v43, |v24|, |v25|, |v26|
	v_max3_f32 v44, |v27|, |v28|, |v29|
	v_max3_f32 v48, |v30|, |v31|, |v32|
	v_max3_f32 v41, v41, v42, |v33|
	v_max3_f32 v43, v43, v44, v48
	v_max_f32_e32 v41, v41, v43
	v_pk_add_f32 v[2:3], v[2:3], v[18:19]
	v_pk_add_f32 v[4:5], v[4:5], v[20:21]
	v_max_f32_dpp v41, v41, v41 quad_perm:[1,0,3,2] row_mask:0xf bank_mask:0xf
	v_pk_add_f32 v[6:7], v[6:7], v[22:23]
	v_pk_add_f32 v[8:9], v[8:9], v[24:25]
	v_max_f32_dpp v41, v41, v41 quad_perm:[2,3,0,1] row_mask:0xf bank_mask:0xf
	v_pk_add_f32 v[10:11], v[10:11], v[26:27]
	v_pk_add_f32 v[12:13], v[12:13], v[28:29]
	v_max_f32_dpp v41, v41, v41 row_half_mirror row_mask:0xf bank_mask:0xf
	v_pk_add_f32 v[14:15], v[14:15], v[30:31]
	v_pk_add_f32 v[16:17], v[16:17], v[32:33]
	v_max_f32_dpp v41, v41, v41 row_mirror row_mask:0xf bank_mask:0xf
	s_nop 1
	v_max_f32_dpp v41, v41, v41 row_bcast:15 row_mask:0xa bank_mask:0xf
	s_nop 1
	v_max_f32_dpp v41, v41, v41 row_bcast:31 row_mask:0xc bank_mask:0xf
	s_nop 1
	v_readlane_b32 s28, v41, 63
	s_nop 1
	v_div_scale_f32 v48, s[30:31], s28, s28, v47
	v_rcp_f32_e32 v49, v48
	s_nop 0
	v_fma_f32 v50, -v48, v49, 1.0
	v_fmac_f32_e32 v49, v50, v49
	v_mov_b32_e32 v50, s28
	v_div_scale_f32 v50, vcc, s32, v50, s32
	v_mul_f32_e32 v51, v50, v49
	v_fma_f32 v52, -v48, v51, v50
	v_fmac_f32_e32 v51, v52, v49
	v_fma_f32 v48, -v48, v51, v50
	v_div_fmas_f32 v48, v48, v49, v51
	v_div_fixup_f32 v48, v48, s28, v47
	v_cmp_gt_f32_e64 vcc, s28, 0
	v_writelane_b32 v40, s28, 8
	s_nop 0
	v_cndmask_b32_e32 v48, 0, v48, vcc
	v_fmaak_f32 v49, v18, v48, 0x4b400000
	v_fmaak_f32 v50, v19, v48, 0x4b400000
	v_fmaak_f32 v51, v20, v48, 0x4b400000
	v_fmaak_f32 v52, v21, v48, 0x4b400000
	v_perm_b32 v49, v50, v49, s33
	v_perm_b32 v51, v52, v51, s34
	v_or_b32_e32 v88, v49, v51
	v_fmaak_f32 v41, v22, v48, 0x4b400000
	v_fmaak_f32 v42, v23, v48, 0x4b400000
	v_fmaak_f32 v43, v24, v48, 0x4b400000
	v_fmaak_f32 v44, v25, v48, 0x4b400000
	v_perm_b32 v41, v42, v41, s33
	v_perm_b32 v43, v44, v43, s34
	v_or_b32_e32 v89, v41, v43
	v_fmaak_f32 v49, v26, v48, 0x4b400000
	v_fmaak_f32 v50, v27, v48, 0x4b400000
	v_fmaak_f32 v51, v28, v48, 0x4b400000
	v_fmaak_f32 v52, v29, v48, 0x4b400000
	v_perm_b32 v49, v50, v49, s33
	v_perm_b32 v51, v52, v51, s34
	v_or_b32_e32 v90, v49, v51
	v_fmaak_f32 v41, v30, v48, 0x4b400000
	v_fmaak_f32 v42, v31, v48, 0x4b400000
	v_fmaak_f32 v43, v32, v48, 0x4b400000
	v_fmaak_f32 v44, v33, v48, 0x4b400000
	v_perm_b32 v41, v42, v41, s33
	v_perm_b32 v43, v44, v43, s34
	v_or_b32_e32 v91, v41, v43
	s_waitcnt vmcnt(0)
	ds_read_b128 v[18:21], v38 offset:4096
	ds_read_b128 v[22:25], v38 offset:5120
	ds_read_b128 v[26:29], v38 offset:6144
	ds_read_b128 v[30:33], v38 offset:7168
	s_waitcnt lgkmcnt(0)
	s_barrier
	s_mov_b32 m0, s35
	s_nop 0
	global_load_lds_dwordx4 v34, s[16:17] nt
	global_load_lds_dwordx4 v34, s[16:17] offset:1024 nt
	global_load_lds_dwordx4 v34, s[16:17] offset:2048 nt
	global_load_lds_dwordx4 v35, s[16:17] offset:3072 nt
	s_add_u32 s16, s16, 0xfa0000
	s_addc_u32 s17, s17, 0
	v_cndmask_b32_e64 v30, 0, v30, s[18:19]
	v_cndmask_b32_e64 v31, 0, v31, s[18:19]
	v_cndmask_b32_e64 v32, 0, v32, s[18:19]
	v_cndmask_b32_e64 v33, 0, v33, s[18:19]
	v_max3_f32 v41, |v18|, |v19|, |v20|
	v_max3_f32 v42, |v21|, |v22|, |v23|
	v_max3_f32 v43, |v24|, |v25|, |v26|
	v_max3_f32 v44, |v27|, |v28|, |v29|
	v_max3_f32 v48, |v30|, |v31|, |v32|
	v_max3_f32 v41, v41, v42, |v33|
	v_max3_f32 v43, v43, v44, v48
	v_max_f32_e32 v41, v41, v43
	v_pk_add_f32 v[2:3], v[2:3], v[18:19]
	v_pk_add_f32 v[4:5], v[4:5], v[20:21]
	v_max_f32_dpp v41, v41, v41 quad_perm:[1,0,3,2] row_mask:0xf bank_mask:0xf
	v_pk_add_f32 v[6:7], v[6:7], v[22:23]
	v_pk_add_f32 v[8:9], v[8:9], v[24:25]
	v_max_f32_dpp v41, v41, v41 quad_perm:[2,3,0,1] row_mask:0xf bank_mask:0xf
	v_pk_add_f32 v[10:11], v[10:11], v[26:27]
	v_pk_add_f32 v[12:13], v[12:13], v[28:29]
	v_max_f32_dpp v41, v41, v41 row_half_mirror row_mask:0xf bank_mask:0xf
	v_pk_add_f32 v[14:15], v[14:15], v[30:31]
	v_pk_add_f32 v[16:17], v[16:17], v[32:33]
	v_max_f32_dpp v41, v41, v41 row_mirror row_mask:0xf bank_mask:0xf
	s_nop 1
	v_max_f32_dpp v41, v41, v41 row_bcast:15 row_mask:0xa bank_mask:0xf
	s_nop 1
	v_max_f32_dpp v41, v41, v41 row_bcast:31 row_mask:0xc bank_mask:0xf
	s_nop 1
	v_readlane_b32 s28, v41, 63
	s_nop 1
	v_div_scale_f32 v48, s[30:31], s28, s28, v47
	v_rcp_f32_e32 v49, v48
	s_nop 0
	v_fma_f32 v50, -v48, v49, 1.0
	v_fmac_f32_e32 v49, v50, v49
	v_mov_b32_e32 v50, s28
	v_div_scale_f32 v50, vcc, s32, v50, s32
	v_mul_f32_e32 v51, v50, v49
	v_fma_f32 v52, -v48, v51, v50
	v_fmac_f32_e32 v51, v52, v49
	v_fma_f32 v48, -v48, v51, v50
	v_div_fmas_f32 v48, v48, v49, v51
	v_div_fixup_f32 v48, v48, s28, v47
	v_cmp_gt_f32_e64 vcc, s28, 0
	v_writelane_b32 v40, s28, 9
	s_nop 0
	v_cndmask_b32_e32 v48, 0, v48, vcc
	v_fmaak_f32 v49, v18, v48, 0x4b400000
	v_fmaak_f32 v50, v19, v48, 0x4b400000
	v_fmaak_f32 v51, v20, v48, 0x4b400000
	v_fmaak_f32 v52, v21, v48, 0x4b400000
	v_perm_b32 v49, v50, v49, s33
	v_perm_b32 v51, v52, v51, s34
	v_or_b32_e32 v92, v49, v51
	v_fmaak_f32 v41, v22, v48, 0x4b400000
	v_fmaak_f32 v42, v23, v48, 0x4b400000
	v_fmaak_f32 v43, v24, v48, 0x4b400000
	v_fmaak_f32 v44, v25, v48, 0x4b400000
	v_perm_b32 v41, v42, v41, s33
	v_perm_b32 v43, v44, v43, s34
	v_or_b32_e32 v93, v41, v43
	v_fmaak_f32 v49, v26, v48, 0x4b400000
	v_fmaak_f32 v50, v27, v48, 0x4b400000
	v_fmaak_f32 v51, v28, v48, 0x4b400000
	v_fmaak_f32 v52, v29, v48, 0x4b400000
	v_perm_b32 v49, v50, v49, s33
	v_perm_b32 v51, v52, v51, s34
	v_or_b32_e32 v94, v49, v51
	v_fmaak_f32 v41, v30, v48, 0x4b400000
	v_fmaak_f32 v42, v31, v48, 0x4b400000
	v_fmaak_f32 v43, v32, v48, 0x4b400000
	v_fmaak_f32 v44, v33, v48, 0x4b400000
	v_perm_b32 v41, v42, v41, s33
	v_perm_b32 v43, v44, v43, s34
	v_or_b32_e32 v95, v41, v43
	s_waitcnt vmcnt(0)
	ds_read_b128 v[18:21], v38 offset:0
	ds_read_b128 v[22:25], v38 offset:1024
	ds_read_b128 v[26:29], v38 offset:2048
	ds_read_b128 v[30:33], v38 offset:3072
	s_waitcnt lgkmcnt(0)
	s_barrier
	s_mov_b32 m0, s36
	s_nop 0
	global_load_lds_dwordx4 v34, s[16:17] nt
	global_load_lds_dwordx4 v34, s[16:17] offset:1024 nt
	global_load_lds_dwordx4 v34, s[16:17] offset:2048 nt
	global_load_lds_dwordx4 v35, s[16:17] offset:3072 nt
	s_add_u32 s16, s16, 0xfa0000
	s_addc_u32 s17, s17, 0
	v_cndmask_b32_e64 v30, 0, v30, s[18:19]
	v_cndmask_b32_e64 v31, 0, v31, s[18:19]
	v_cndmask_b32_e64 v32, 0, v32, s[18:19]
	v_cndmask_b32_e64 v33, 0, v33, s[18:19]
	v_max3_f32 v41, |v18|, |v19|, |v20|
	v_max3_f32 v42, |v21|, |v22|, |v23|
	v_max3_f32 v43, |v24|, |v25|, |v26|
	v_max3_f32 v44, |v27|, |v28|, |v29|
	v_max3_f32 v48, |v30|, |v31|, |v32|
	v_max3_f32 v41, v41, v42, |v33|
	v_max3_f32 v43, v43, v44, v48
	v_max_f32_e32 v41, v41, v43
	v_pk_add_f32 v[2:3], v[2:3], v[18:19]
	v_pk_add_f32 v[4:5], v[4:5], v[20:21]
	v_max_f32_dpp v41, v41, v41 quad_perm:[1,0,3,2] row_mask:0xf bank_mask:0xf
	v_pk_add_f32 v[6:7], v[6:7], v[22:23]
	v_pk_add_f32 v[8:9], v[8:9], v[24:25]
	v_max_f32_dpp v41, v41, v41 quad_perm:[2,3,0,1] row_mask:0xf bank_mask:0xf
	v_pk_add_f32 v[10:11], v[10:11], v[26:27]
	v_pk_add_f32 v[12:13], v[12:13], v[28:29]
	v_max_f32_dpp v41, v41, v41 row_half_mirror row_mask:0xf bank_mask:0xf
	v_pk_add_f32 v[14:15], v[14:15], v[30:31]
	v_pk_add_f32 v[16:17], v[16:17], v[32:33]
	v_max_f32_dpp v41, v41, v41 row_mirror row_mask:0xf bank_mask:0xf
	s_nop 1
	v_max_f32_dpp v41, v41, v41 row_bcast:15 row_mask:0xa bank_mask:0xf
	s_nop 1
	v_max_f32_dpp v41, v41, v41 row_bcast:31 row_mask:0xc bank_mask:0xf
	s_nop 1
	v_readlane_b32 s28, v41, 63
	s_nop 1
	v_div_scale_f32 v48, s[30:31], s28, s28, v47
	v_rcp_f32_e32 v49, v48
	s_nop 0
	v_fma_f32 v50, -v48, v49, 1.0
	v_fmac_f32_e32 v49, v50, v49
	v_mov_b32_e32 v50, s28
	v_div_scale_f32 v50, vcc, s32, v50, s32
	v_mul_f32_e32 v51, v50, v49
	v_fma_f32 v52, -v48, v51, v50
	v_fmac_f32_e32 v51, v52, v49
	v_fma_f32 v48, -v48, v51, v50
	v_div_fmas_f32 v48, v48, v49, v51
	v_div_fixup_f32 v48, v48, s28, v47
	v_cmp_gt_f32_e64 vcc, s28, 0
	v_writelane_b32 v40, s28, 10
	s_nop 0
	v_cndmask_b32_e32 v48, 0, v48, vcc
	v_fmaak_f32 v49, v18, v48, 0x4b400000
	v_fmaak_f32 v50, v19, v48, 0x4b400000
	v_fmaak_f32 v51, v20, v48, 0x4b400000
	v_fmaak_f32 v52, v21, v48, 0x4b400000
	v_perm_b32 v49, v50, v49, s33
	v_perm_b32 v51, v52, v51, s34
	v_or_b32_e32 v96, v49, v51
	v_fmaak_f32 v41, v22, v48, 0x4b400000
	v_fmaak_f32 v42, v23, v48, 0x4b400000
	v_fmaak_f32 v43, v24, v48, 0x4b400000
	v_fmaak_f32 v44, v25, v48, 0x4b400000
	v_perm_b32 v41, v42, v41, s33
	v_perm_b32 v43, v44, v43, s34
	v_or_b32_e32 v97, v41, v43
	v_fmaak_f32 v49, v26, v48, 0x4b400000
	v_fmaak_f32 v50, v27, v48, 0x4b400000
	v_fmaak_f32 v51, v28, v48, 0x4b400000
	v_fmaak_f32 v52, v29, v48, 0x4b400000
	v_perm_b32 v49, v50, v49, s33
	v_perm_b32 v51, v52, v51, s34
	v_or_b32_e32 v98, v49, v51
	v_fmaak_f32 v41, v30, v48, 0x4b400000
	v_fmaak_f32 v42, v31, v48, 0x4b400000
	v_fmaak_f32 v43, v32, v48, 0x4b400000
	v_fmaak_f32 v44, v33, v48, 0x4b400000
	v_perm_b32 v41, v42, v41, s33
	v_perm_b32 v43, v44, v43, s34
	v_or_b32_e32 v99, v41, v43
	s_waitcnt vmcnt(0)
	ds_read_b128 v[18:21], v38 offset:4096
	ds_read_b128 v[22:25], v38 offset:5120
	ds_read_b128 v[26:29], v38 offset:6144
	ds_read_b128 v[30:33], v38 offset:7168
	s_waitcnt lgkmcnt(0)
	s_barrier
	s_mov_b32 m0, s35
	s_nop 0
	global_load_lds_dwordx4 v34, s[16:17] nt
	global_load_lds_dwordx4 v34, s[16:17] offset:1024 nt
	global_load_lds_dwordx4 v34, s[16:17] offset:2048 nt
	global_load_lds_dwordx4 v35, s[16:17] offset:3072 nt
	s_add_u32 s16, s16, 0xfa0000
	s_addc_u32 s17, s17, 0
	v_cndmask_b32_e64 v30, 0, v30, s[18:19]
	v_cndmask_b32_e64 v31, 0, v31, s[18:19]
	v_cndmask_b32_e64 v32, 0, v32, s[18:19]
	v_cndmask_b32_e64 v33, 0, v33, s[18:19]
	v_max3_f32 v41, |v18|, |v19|, |v20|
	v_max3_f32 v42, |v21|, |v22|, |v23|
	v_max3_f32 v43, |v24|, |v25|, |v26|
	v_max3_f32 v44, |v27|, |v28|, |v29|
	v_max3_f32 v48, |v30|, |v31|, |v32|
	v_max3_f32 v41, v41, v42, |v33|
	v_max3_f32 v43, v43, v44, v48
	v_max_f32_e32 v41, v41, v43
	v_pk_add_f32 v[2:3], v[2:3], v[18:19]
	v_pk_add_f32 v[4:5], v[4:5], v[20:21]
	v_max_f32_dpp v41, v41, v41 quad_perm:[1,0,3,2] row_mask:0xf bank_mask:0xf
	v_pk_add_f32 v[6:7], v[6:7], v[22:23]
	v_pk_add_f32 v[8:9], v[8:9], v[24:25]
	v_max_f32_dpp v41, v41, v41 quad_perm:[2,3,0,1] row_mask:0xf bank_mask:0xf
	v_pk_add_f32 v[10:11], v[10:11], v[26:27]
	v_pk_add_f32 v[12:13], v[12:13], v[28:29]
	v_max_f32_dpp v41, v41, v41 row_half_mirror row_mask:0xf bank_mask:0xf
	v_pk_add_f32 v[14:15], v[14:15], v[30:31]
	v_pk_add_f32 v[16:17], v[16:17], v[32:33]
	v_max_f32_dpp v41, v41, v41 row_mirror row_mask:0xf bank_mask:0xf
	s_nop 1
	v_max_f32_dpp v41, v41, v41 row_bcast:15 row_mask:0xa bank_mask:0xf
	s_nop 1
	v_max_f32_dpp v41, v41, v41 row_bcast:31 row_mask:0xc bank_mask:0xf
	s_nop 1
	v_readlane_b32 s28, v41, 63
	s_nop 1
	v_div_scale_f32 v48, s[30:31], s28, s28, v47
	v_rcp_f32_e32 v49, v48
	s_nop 0
	v_fma_f32 v50, -v48, v49, 1.0
	v_fmac_f32_e32 v49, v50, v49
	v_mov_b32_e32 v50, s28
	v_div_scale_f32 v50, vcc, s32, v50, s32
	v_mul_f32_e32 v51, v50, v49
	v_fma_f32 v52, -v48, v51, v50
	v_fmac_f32_e32 v51, v52, v49
	v_fma_f32 v48, -v48, v51, v50
	v_div_fmas_f32 v48, v48, v49, v51
	v_div_fixup_f32 v48, v48, s28, v47
	v_cmp_gt_f32_e64 vcc, s28, 0
	v_writelane_b32 v40, s28, 11
	s_nop 0
	v_cndmask_b32_e32 v48, 0, v48, vcc
	v_fmaak_f32 v49, v18, v48, 0x4b400000
	v_fmaak_f32 v50, v19, v48, 0x4b400000
	v_fmaak_f32 v51, v20, v48, 0x4b400000
	v_fmaak_f32 v52, v21, v48, 0x4b400000
	v_perm_b32 v49, v50, v49, s33
	v_perm_b32 v51, v52, v51, s34
	v_or_b32_e32 v100, v49, v51
	v_fmaak_f32 v41, v22, v48, 0x4b400000
	v_fmaak_f32 v42, v23, v48, 0x4b400000
	v_fmaak_f32 v43, v24, v48, 0x4b400000
	v_fmaak_f32 v44, v25, v48, 0x4b400000
	v_perm_b32 v41, v42, v41, s33
	v_perm_b32 v43, v44, v43, s34
	v_or_b32_e32 v101, v41, v43
	v_fmaak_f32 v49, v26, v48, 0x4b400000
	v_fmaak_f32 v50, v27, v48, 0x4b400000
	v_fmaak_f32 v51, v28, v48, 0x4b400000
	v_fmaak_f32 v52, v29, v48, 0x4b400000
	v_perm_b32 v49, v50, v49, s33
	v_perm_b32 v51, v52, v51, s34
	v_or_b32_e32 v102, v49, v51
	v_fmaak_f32 v41, v30, v48, 0x4b400000
	v_fmaak_f32 v42, v31, v48, 0x4b400000
	v_fmaak_f32 v43, v32, v48, 0x4b400000
	v_fmaak_f32 v44, v33, v48, 0x4b400000
	v_perm_b32 v41, v42, v41, s33
	v_perm_b32 v43, v44, v43, s34
	v_or_b32_e32 v103, v41, v43
	s_waitcnt vmcnt(0)
	ds_read_b128 v[18:21], v38 offset:0
	ds_read_b128 v[22:25], v38 offset:1024
	ds_read_b128 v[26:29], v38 offset:2048
	ds_read_b128 v[30:33], v38 offset:3072
	s_waitcnt lgkmcnt(0)
	s_barrier
	s_mov_b32 m0, s36
	s_nop 0
	global_load_lds_dwordx4 v34, s[16:17] nt
	global_load_lds_dwordx4 v34, s[16:17] offset:1024 nt
	global_load_lds_dwordx4 v34, s[16:17] offset:2048 nt
	global_load_lds_dwordx4 v35, s[16:17] offset:3072 nt
	s_add_u32 s16, s16, 0xfa0000
	s_addc_u32 s17, s17, 0
	v_cndmask_b32_e64 v30, 0, v30, s[18:19]
	v_cndmask_b32_e64 v31, 0, v31, s[18:19]
	v_cndmask_b32_e64 v32, 0, v32, s[18:19]
	v_cndmask_b32_e64 v33, 0, v33, s[18:19]
	v_max3_f32 v41, |v18|, |v19|, |v20|
	v_max3_f32 v42, |v21|, |v22|, |v23|
	v_max3_f32 v43, |v24|, |v25|, |v26|
	v_max3_f32 v44, |v27|, |v28|, |v29|
	v_max3_f32 v48, |v30|, |v31|, |v32|
	v_max3_f32 v41, v41, v42, |v33|
	v_max3_f32 v43, v43, v44, v48
	v_max_f32_e32 v41, v41, v43
	v_pk_add_f32 v[2:3], v[2:3], v[18:19]
	v_pk_add_f32 v[4:5], v[4:5], v[20:21]
	v_max_f32_dpp v41, v41, v41 quad_perm:[1,0,3,2] row_mask:0xf bank_mask:0xf
	v_pk_add_f32 v[6:7], v[6:7], v[22:23]
	v_pk_add_f32 v[8:9], v[8:9], v[24:25]
	v_max_f32_dpp v41, v41, v41 quad_perm:[2,3,0,1] row_mask:0xf bank_mask:0xf
	v_pk_add_f32 v[10:11], v[10:11], v[26:27]
	v_pk_add_f32 v[12:13], v[12:13], v[28:29]
	v_max_f32_dpp v41, v41, v41 row_half_mirror row_mask:0xf bank_mask:0xf
	v_pk_add_f32 v[14:15], v[14:15], v[30:31]
	v_pk_add_f32 v[16:17], v[16:17], v[32:33]
	v_max_f32_dpp v41, v41, v41 row_mirror row_mask:0xf bank_mask:0xf
	s_nop 1
	v_max_f32_dpp v41, v41, v41 row_bcast:15 row_mask:0xa bank_mask:0xf
	s_nop 1
	v_max_f32_dpp v41, v41, v41 row_bcast:31 row_mask:0xc bank_mask:0xf
	s_nop 1
	v_readlane_b32 s28, v41, 63
	s_nop 1
	v_div_scale_f32 v48, s[30:31], s28, s28, v47
	v_rcp_f32_e32 v49, v48
	s_nop 0
	v_fma_f32 v50, -v48, v49, 1.0
	v_fmac_f32_e32 v49, v50, v49
	v_mov_b32_e32 v50, s28
	v_div_scale_f32 v50, vcc, s32, v50, s32
	v_mul_f32_e32 v51, v50, v49
	v_fma_f32 v52, -v48, v51, v50
	v_fmac_f32_e32 v51, v52, v49
	v_fma_f32 v48, -v48, v51, v50
	v_div_fmas_f32 v48, v48, v49, v51
	v_div_fixup_f32 v48, v48, s28, v47
	v_cmp_gt_f32_e64 vcc, s28, 0
	v_writelane_b32 v40, s28, 12
	s_nop 0
	v_cndmask_b32_e32 v48, 0, v48, vcc
	v_fmaak_f32 v49, v18, v48, 0x4b400000
	v_fmaak_f32 v50, v19, v48, 0x4b400000
	v_fmaak_f32 v51, v20, v48, 0x4b400000
	v_fmaak_f32 v52, v21, v48, 0x4b400000
	v_perm_b32 v49, v50, v49, s33
	v_perm_b32 v51, v52, v51, s34
	v_or_b32_e32 v104, v49, v51
	v_fmaak_f32 v41, v22, v48, 0x4b400000
	v_fmaak_f32 v42, v23, v48, 0x4b400000
	v_fmaak_f32 v43, v24, v48, 0x4b400000
	v_fmaak_f32 v44, v25, v48, 0x4b400000
	v_perm_b32 v41, v42, v41, s33
	v_perm_b32 v43, v44, v43, s34
	v_or_b32_e32 v105, v41, v43
	v_fmaak_f32 v49, v26, v48, 0x4b400000
	v_fmaak_f32 v50, v27, v48, 0x4b400000
	v_fmaak_f32 v51, v28, v48, 0x4b400000
	v_fmaak_f32 v52, v29, v48, 0x4b400000
	v_perm_b32 v49, v50, v49, s33
	v_perm_b32 v51, v52, v51, s34
	v_or_b32_e32 v106, v49, v51
	v_fmaak_f32 v41, v30, v48, 0x4b400000
	v_fmaak_f32 v42, v31, v48, 0x4b400000
	v_fmaak_f32 v43, v32, v48, 0x4b400000
	v_fmaak_f32 v44, v33, v48, 0x4b400000
	v_perm_b32 v41, v42, v41, s33
	v_perm_b32 v43, v44, v43, s34
	v_or_b32_e32 v107, v41, v43
	s_waitcnt vmcnt(0)
	ds_read_b128 v[18:21], v38 offset:4096
	ds_read_b128 v[22:25], v38 offset:5120
	ds_read_b128 v[26:29], v38 offset:6144
	ds_read_b128 v[30:33], v38 offset:7168
	s_waitcnt lgkmcnt(0)
	s_barrier
	s_mov_b32 m0, s35
	s_nop 0
	global_load_lds_dwordx4 v34, s[16:17] nt
	global_load_lds_dwordx4 v34, s[16:17] offset:1024 nt
	global_load_lds_dwordx4 v34, s[16:17] offset:2048 nt
	global_load_lds_dwordx4 v35, s[16:17] offset:3072 nt
	s_add_u32 s16, s16, 0xfa0000
	s_addc_u32 s17, s17, 0
	v_cndmask_b32_e64 v30, 0, v30, s[18:19]
	v_cndmask_b32_e64 v31, 0, v31, s[18:19]
	v_cndmask_b32_e64 v32, 0, v32, s[18:19]
	v_cndmask_b32_e64 v33, 0, v33, s[18:19]
	v_max3_f32 v41, |v18|, |v19|, |v20|
	v_max3_f32 v42, |v21|, |v22|, |v23|
	v_max3_f32 v43, |v24|, |v25|, |v26|
	v_max3_f32 v44, |v27|, |v28|, |v29|
	v_max3_f32 v48, |v30|, |v31|, |v32|
	v_max3_f32 v41, v41, v42, |v33|
	v_max3_f32 v43, v43, v44, v48
	v_max_f32_e32 v41, v41, v43
	v_pk_add_f32 v[2:3], v[2:3], v[18:19]
	v_pk_add_f32 v[4:5], v[4:5], v[20:21]
	v_max_f32_dpp v41, v41, v41 quad_perm:[1,0,3,2] row_mask:0xf bank_mask:0xf
	v_pk_add_f32 v[6:7], v[6:7], v[22:23]
	v_pk_add_f32 v[8:9], v[8:9], v[24:25]
	v_max_f32_dpp v41, v41, v41 quad_perm:[2,3,0,1] row_mask:0xf bank_mask:0xf
	v_pk_add_f32 v[10:11], v[10:11], v[26:27]
	v_pk_add_f32 v[12:13], v[12:13], v[28:29]
	v_max_f32_dpp v41, v41, v41 row_half_mirror row_mask:0xf bank_mask:0xf
	v_pk_add_f32 v[14:15], v[14:15], v[30:31]
	v_pk_add_f32 v[16:17], v[16:17], v[32:33]
	v_max_f32_dpp v41, v41, v41 row_mirror row_mask:0xf bank_mask:0xf
	s_nop 1
	v_max_f32_dpp v41, v41, v41 row_bcast:15 row_mask:0xa bank_mask:0xf
	s_nop 1
	v_max_f32_dpp v41, v41, v41 row_bcast:31 row_mask:0xc bank_mask:0xf
	s_nop 1
	v_readlane_b32 s28, v41, 63
	s_nop 1
	v_div_scale_f32 v48, s[30:31], s28, s28, v47
	v_rcp_f32_e32 v49, v48
	s_nop 0
	v_fma_f32 v50, -v48, v49, 1.0
	v_fmac_f32_e32 v49, v50, v49
	v_mov_b32_e32 v50, s28
	v_div_scale_f32 v50, vcc, s32, v50, s32
	v_mul_f32_e32 v51, v50, v49
	v_fma_f32 v52, -v48, v51, v50
	v_fmac_f32_e32 v51, v52, v49
	v_fma_f32 v48, -v48, v51, v50
	v_div_fmas_f32 v48, v48, v49, v51
	v_div_fixup_f32 v48, v48, s28, v47
	v_cmp_gt_f32_e64 vcc, s28, 0
	v_writelane_b32 v40, s28, 13
	s_nop 0
	v_cndmask_b32_e32 v48, 0, v48, vcc
	v_fmaak_f32 v49, v18, v48, 0x4b400000
	v_fmaak_f32 v50, v19, v48, 0x4b400000
	v_fmaak_f32 v51, v20, v48, 0x4b400000
	v_fmaak_f32 v52, v21, v48, 0x4b400000
	v_perm_b32 v49, v50, v49, s33
	v_perm_b32 v51, v52, v51, s34
	v_or_b32_e32 v108, v49, v51
	v_fmaak_f32 v41, v22, v48, 0x4b400000
	v_fmaak_f32 v42, v23, v48, 0x4b400000
	v_fmaak_f32 v43, v24, v48, 0x4b400000
	v_fmaak_f32 v44, v25, v48, 0x4b400000
	v_perm_b32 v41, v42, v41, s33
	v_perm_b32 v43, v44, v43, s34
	v_or_b32_e32 v109, v41, v43
	v_fmaak_f32 v49, v26, v48, 0x4b400000
	v_fmaak_f32 v50, v27, v48, 0x4b400000
	v_fmaak_f32 v51, v28, v48, 0x4b400000
	v_fmaak_f32 v52, v29, v48, 0x4b400000
	v_perm_b32 v49, v50, v49, s33
	v_perm_b32 v51, v52, v51, s34
	v_or_b32_e32 v110, v49, v51
	v_fmaak_f32 v41, v30, v48, 0x4b400000
	v_fmaak_f32 v42, v31, v48, 0x4b400000
	v_fmaak_f32 v43, v32, v48, 0x4b400000
	v_fmaak_f32 v44, v33, v48, 0x4b400000
	v_perm_b32 v41, v42, v41, s33
	v_perm_b32 v43, v44, v43, s34
	v_or_b32_e32 v111, v41, v43
	s_waitcnt vmcnt(0)
	ds_read_b128 v[18:21], v38 offset:0
	ds_read_b128 v[22:25], v38 offset:1024
	ds_read_b128 v[26:29], v38 offset:2048
	ds_read_b128 v[30:33], v38 offset:3072
	s_waitcnt lgkmcnt(0)
	s_barrier
	s_mov_b32 m0, s36
	s_nop 0
	global_load_lds_dwordx4 v34, s[16:17] nt
	global_load_lds_dwordx4 v34, s[16:17] offset:1024 nt
	global_load_lds_dwordx4 v34, s[16:17] offset:2048 nt
	global_load_lds_dwordx4 v35, s[16:17] offset:3072 nt
	s_add_u32 s16, s16, 0xfa0000
	s_addc_u32 s17, s17, 0
	v_cndmask_b32_e64 v30, 0, v30, s[18:19]
	v_cndmask_b32_e64 v31, 0, v31, s[18:19]
	v_cndmask_b32_e64 v32, 0, v32, s[18:19]
	v_cndmask_b32_e64 v33, 0, v33, s[18:19]
	v_max3_f32 v41, |v18|, |v19|, |v20|
	v_max3_f32 v42, |v21|, |v22|, |v23|
	v_max3_f32 v43, |v24|, |v25|, |v26|
	v_max3_f32 v44, |v27|, |v28|, |v29|
	v_max3_f32 v48, |v30|, |v31|, |v32|
	v_max3_f32 v41, v41, v42, |v33|
	v_max3_f32 v43, v43, v44, v48
	v_max_f32_e32 v41, v41, v43
	v_pk_add_f32 v[2:3], v[2:3], v[18:19]
	v_pk_add_f32 v[4:5], v[4:5], v[20:21]
	v_max_f32_dpp v41, v41, v41 quad_perm:[1,0,3,2] row_mask:0xf bank_mask:0xf
	v_pk_add_f32 v[6:7], v[6:7], v[22:23]
	v_pk_add_f32 v[8:9], v[8:9], v[24:25]
	v_max_f32_dpp v41, v41, v41 quad_perm:[2,3,0,1] row_mask:0xf bank_mask:0xf
	v_pk_add_f32 v[10:11], v[10:11], v[26:27]
	v_pk_add_f32 v[12:13], v[12:13], v[28:29]
	v_max_f32_dpp v41, v41, v41 row_half_mirror row_mask:0xf bank_mask:0xf
	v_pk_add_f32 v[14:15], v[14:15], v[30:31]
	v_pk_add_f32 v[16:17], v[16:17], v[32:33]
	v_max_f32_dpp v41, v41, v41 row_mirror row_mask:0xf bank_mask:0xf
	s_nop 1
	v_max_f32_dpp v41, v41, v41 row_bcast:15 row_mask:0xa bank_mask:0xf
	s_nop 1
	v_max_f32_dpp v41, v41, v41 row_bcast:31 row_mask:0xc bank_mask:0xf
	s_nop 1
	v_readlane_b32 s28, v41, 63
	s_nop 1
	v_div_scale_f32 v48, s[30:31], s28, s28, v47
	v_rcp_f32_e32 v49, v48
	s_nop 0
	v_fma_f32 v50, -v48, v49, 1.0
	v_fmac_f32_e32 v49, v50, v49
	v_mov_b32_e32 v50, s28
	v_div_scale_f32 v50, vcc, s32, v50, s32
	v_mul_f32_e32 v51, v50, v49
	v_fma_f32 v52, -v48, v51, v50
	v_fmac_f32_e32 v51, v52, v49
	v_fma_f32 v48, -v48, v51, v50
	v_div_fmas_f32 v48, v48, v49, v51
	v_div_fixup_f32 v48, v48, s28, v47
	v_cmp_gt_f32_e64 vcc, s28, 0
	v_writelane_b32 v40, s28, 14
	s_nop 0
	v_cndmask_b32_e32 v48, 0, v48, vcc
	v_fmaak_f32 v49, v18, v48, 0x4b400000
	v_fmaak_f32 v50, v19, v48, 0x4b400000
	v_fmaak_f32 v51, v20, v48, 0x4b400000
	v_fmaak_f32 v52, v21, v48, 0x4b400000
	v_perm_b32 v49, v50, v49, s33
	v_perm_b32 v51, v52, v51, s34
	v_or_b32_e32 v112, v49, v51
	v_fmaak_f32 v41, v22, v48, 0x4b400000
	v_fmaak_f32 v42, v23, v48, 0x4b400000
	v_fmaak_f32 v43, v24, v48, 0x4b400000
	v_fmaak_f32 v44, v25, v48, 0x4b400000
	v_perm_b32 v41, v42, v41, s33
	v_perm_b32 v43, v44, v43, s34
	v_or_b32_e32 v113, v41, v43
	v_fmaak_f32 v49, v26, v48, 0x4b400000
	v_fmaak_f32 v50, v27, v48, 0x4b400000
	v_fmaak_f32 v51, v28, v48, 0x4b400000
	v_fmaak_f32 v52, v29, v48, 0x4b400000
	v_perm_b32 v49, v50, v49, s33
	v_perm_b32 v51, v52, v51, s34
	v_or_b32_e32 v114, v49, v51
	v_fmaak_f32 v41, v30, v48, 0x4b400000
	v_fmaak_f32 v42, v31, v48, 0x4b400000
	v_fmaak_f32 v43, v32, v48, 0x4b400000
	v_fmaak_f32 v44, v33, v48, 0x4b400000
	v_perm_b32 v41, v42, v41, s33
	v_perm_b32 v43, v44, v43, s34
	v_or_b32_e32 v115, v41, v43
	s_waitcnt vmcnt(0)
	ds_read_b128 v[18:21], v38 offset:4096
	ds_read_b128 v[22:25], v38 offset:5120
	ds_read_b128 v[26:29], v38 offset:6144
	ds_read_b128 v[30:33], v38 offset:7168
	s_waitcnt lgkmcnt(0)
	s_barrier
	s_mov_b32 m0, s35
	s_nop 0
	global_load_lds_dwordx4 v34, s[16:17] nt
	global_load_lds_dwordx4 v34, s[16:17] offset:1024 nt
	global_load_lds_dwordx4 v34, s[16:17] offset:2048 nt
	global_load_lds_dwordx4 v35, s[16:17] offset:3072 nt
	s_add_u32 s16, s16, 0xfa0000
	s_addc_u32 s17, s17, 0
	v_cndmask_b32_e64 v30, 0, v30, s[18:19]
	v_cndmask_b32_e64 v31, 0, v31, s[18:19]
	v_cndmask_b32_e64 v32, 0, v32, s[18:19]
	v_cndmask_b32_e64 v33, 0, v33, s[18:19]
	v_max3_f32 v41, |v18|, |v19|, |v20|
	v_max3_f32 v42, |v21|, |v22|, |v23|
	v_max3_f32 v43, |v24|, |v25|, |v26|
	v_max3_f32 v44, |v27|, |v28|, |v29|
	v_max3_f32 v48, |v30|, |v31|, |v32|
	v_max3_f32 v41, v41, v42, |v33|
	v_max3_f32 v43, v43, v44, v48
	v_max_f32_e32 v41, v41, v43
	v_pk_add_f32 v[2:3], v[2:3], v[18:19]
	v_pk_add_f32 v[4:5], v[4:5], v[20:21]
	v_max_f32_dpp v41, v41, v41 quad_perm:[1,0,3,2] row_mask:0xf bank_mask:0xf
	v_pk_add_f32 v[6:7], v[6:7], v[22:23]
	v_pk_add_f32 v[8:9], v[8:9], v[24:25]
	v_max_f32_dpp v41, v41, v41 quad_perm:[2,3,0,1] row_mask:0xf bank_mask:0xf
	v_pk_add_f32 v[10:11], v[10:11], v[26:27]
	v_pk_add_f32 v[12:13], v[12:13], v[28:29]
	v_max_f32_dpp v41, v41, v41 row_half_mirror row_mask:0xf bank_mask:0xf
	v_pk_add_f32 v[14:15], v[14:15], v[30:31]
	v_pk_add_f32 v[16:17], v[16:17], v[32:33]
	v_max_f32_dpp v41, v41, v41 row_mirror row_mask:0xf bank_mask:0xf
	s_nop 1
	v_max_f32_dpp v41, v41, v41 row_bcast:15 row_mask:0xa bank_mask:0xf
	s_nop 1
	v_max_f32_dpp v41, v41, v41 row_bcast:31 row_mask:0xc bank_mask:0xf
	s_nop 1
	v_readlane_b32 s28, v41, 63
	s_nop 1
	v_div_scale_f32 v48, s[30:31], s28, s28, v47
	v_rcp_f32_e32 v49, v48
	s_nop 0
	v_fma_f32 v50, -v48, v49, 1.0
	v_fmac_f32_e32 v49, v50, v49
	v_mov_b32_e32 v50, s28
	v_div_scale_f32 v50, vcc, s32, v50, s32
	v_mul_f32_e32 v51, v50, v49
	v_fma_f32 v52, -v48, v51, v50
	v_fmac_f32_e32 v51, v52, v49
	v_fma_f32 v48, -v48, v51, v50
	v_div_fmas_f32 v48, v48, v49, v51
	v_div_fixup_f32 v48, v48, s28, v47
	v_cmp_gt_f32_e64 vcc, s28, 0
	v_writelane_b32 v40, s28, 15
	s_nop 0
	v_cndmask_b32_e32 v48, 0, v48, vcc
	v_fmaak_f32 v49, v18, v48, 0x4b400000
	v_fmaak_f32 v50, v19, v48, 0x4b400000
	v_fmaak_f32 v51, v20, v48, 0x4b400000
	v_fmaak_f32 v52, v21, v48, 0x4b400000
	v_perm_b32 v49, v50, v49, s33
	v_perm_b32 v51, v52, v51, s34
	v_or_b32_e32 v116, v49, v51
	v_fmaak_f32 v41, v22, v48, 0x4b400000
	v_fmaak_f32 v42, v23, v48, 0x4b400000
	v_fmaak_f32 v43, v24, v48, 0x4b400000
	v_fmaak_f32 v44, v25, v48, 0x4b400000
	v_perm_b32 v41, v42, v41, s33
	v_perm_b32 v43, v44, v43, s34
	v_or_b32_e32 v117, v41, v43
	v_fmaak_f32 v49, v26, v48, 0x4b400000
	v_fmaak_f32 v50, v27, v48, 0x4b400000
	v_fmaak_f32 v51, v28, v48, 0x4b400000
	v_fmaak_f32 v52, v29, v48, 0x4b400000
	v_perm_b32 v49, v50, v49, s33
	v_perm_b32 v51, v52, v51, s34
	v_or_b32_e32 v118, v49, v51
	v_fmaak_f32 v41, v30, v48, 0x4b400000
	v_fmaak_f32 v42, v31, v48, 0x4b400000
	v_fmaak_f32 v43, v32, v48, 0x4b400000
	v_fmaak_f32 v44, v33, v48, 0x4b400000
	v_perm_b32 v41, v42, v41, s33
	v_perm_b32 v43, v44, v43, s34
	v_or_b32_e32 v119, v41, v43
	s_waitcnt vmcnt(0)
	ds_read_b128 v[18:21], v38 offset:0
	ds_read_b128 v[22:25], v38 offset:1024
	ds_read_b128 v[26:29], v38 offset:2048
	ds_read_b128 v[30:33], v38 offset:3072
	s_waitcnt lgkmcnt(0)
	s_barrier
	s_mov_b32 m0, s36
	s_nop 0
	global_load_lds_dwordx4 v34, s[16:17] nt
	global_load_lds_dwordx4 v34, s[16:17] offset:1024 nt
	global_load_lds_dwordx4 v34, s[16:17] offset:2048 nt
	global_load_lds_dwordx4 v35, s[16:17] offset:3072 nt
	s_add_u32 s16, s16, 0xfa0000
	s_addc_u32 s17, s17, 0
	v_cndmask_b32_e64 v30, 0, v30, s[18:19]
	v_cndmask_b32_e64 v31, 0, v31, s[18:19]
	v_cndmask_b32_e64 v32, 0, v32, s[18:19]
	v_cndmask_b32_e64 v33, 0, v33, s[18:19]
	v_max3_f32 v41, |v18|, |v19|, |v20|
	v_max3_f32 v42, |v21|, |v22|, |v23|
	v_max3_f32 v43, |v24|, |v25|, |v26|
	v_max3_f32 v44, |v27|, |v28|, |v29|
	v_max3_f32 v48, |v30|, |v31|, |v32|
	v_max3_f32 v41, v41, v42, |v33|
	v_max3_f32 v43, v43, v44, v48
	v_max_f32_e32 v41, v41, v43
	v_pk_add_f32 v[2:3], v[2:3], v[18:19]
	v_pk_add_f32 v[4:5], v[4:5], v[20:21]
	v_max_f32_dpp v41, v41, v41 quad_perm:[1,0,3,2] row_mask:0xf bank_mask:0xf
	v_pk_add_f32 v[6:7], v[6:7], v[22:23]
	v_pk_add_f32 v[8:9], v[8:9], v[24:25]
	v_max_f32_dpp v41, v41, v41 quad_perm:[2,3,0,1] row_mask:0xf bank_mask:0xf
	v_pk_add_f32 v[10:11], v[10:11], v[26:27]
	v_pk_add_f32 v[12:13], v[12:13], v[28:29]
	v_max_f32_dpp v41, v41, v41 row_half_mirror row_mask:0xf bank_mask:0xf
	v_pk_add_f32 v[14:15], v[14:15], v[30:31]
	v_pk_add_f32 v[16:17], v[16:17], v[32:33]
	v_max_f32_dpp v41, v41, v41 row_mirror row_mask:0xf bank_mask:0xf
	s_nop 1
	v_max_f32_dpp v41, v41, v41 row_bcast:15 row_mask:0xa bank_mask:0xf
	s_nop 1
	v_max_f32_dpp v41, v41, v41 row_bcast:31 row_mask:0xc bank_mask:0xf
	s_nop 1
	v_readlane_b32 s28, v41, 63
	s_nop 1
	v_div_scale_f32 v48, s[30:31], s28, s28, v47
	v_rcp_f32_e32 v49, v48
	s_nop 0
	v_fma_f32 v50, -v48, v49, 1.0
	v_fmac_f32_e32 v49, v50, v49
	v_mov_b32_e32 v50, s28
	v_div_scale_f32 v50, vcc, s32, v50, s32
	v_mul_f32_e32 v51, v50, v49
	v_fma_f32 v52, -v48, v51, v50
	v_fmac_f32_e32 v51, v52, v49
	v_fma_f32 v48, -v48, v51, v50
	v_div_fmas_f32 v48, v48, v49, v51
	v_div_fixup_f32 v48, v48, s28, v47
	v_cmp_gt_f32_e64 vcc, s28, 0
	v_writelane_b32 v40, s28, 16
	s_nop 0
	v_cndmask_b32_e32 v48, 0, v48, vcc
	v_fmaak_f32 v49, v18, v48, 0x4b400000
	v_fmaak_f32 v50, v19, v48, 0x4b400000
	v_fmaak_f32 v51, v20, v48, 0x4b400000
	v_fmaak_f32 v52, v21, v48, 0x4b400000
	v_perm_b32 v49, v50, v49, s33
	v_perm_b32 v51, v52, v51, s34
	v_or_b32_e32 v120, v49, v51
	v_fmaak_f32 v41, v22, v48, 0x4b400000
	v_fmaak_f32 v42, v23, v48, 0x4b400000
	v_fmaak_f32 v43, v24, v48, 0x4b400000
	v_fmaak_f32 v44, v25, v48, 0x4b400000
	v_perm_b32 v41, v42, v41, s33
	v_perm_b32 v43, v44, v43, s34
	v_or_b32_e32 v121, v41, v43
	v_fmaak_f32 v49, v26, v48, 0x4b400000
	v_fmaak_f32 v50, v27, v48, 0x4b400000
	v_fmaak_f32 v51, v28, v48, 0x4b400000
	v_fmaak_f32 v52, v29, v48, 0x4b400000
	v_perm_b32 v49, v50, v49, s33
	v_perm_b32 v51, v52, v51, s34
	v_or_b32_e32 v122, v49, v51
	v_fmaak_f32 v41, v30, v48, 0x4b400000
	v_fmaak_f32 v42, v31, v48, 0x4b400000
	v_fmaak_f32 v43, v32, v48, 0x4b400000
	v_fmaak_f32 v44, v33, v48, 0x4b400000
	v_perm_b32 v41, v42, v41, s33
	v_perm_b32 v43, v44, v43, s34
	v_or_b32_e32 v123, v41, v43
	s_waitcnt vmcnt(0)
	ds_read_b128 v[18:21], v38 offset:4096
	ds_read_b128 v[22:25], v38 offset:5120
	ds_read_b128 v[26:29], v38 offset:6144
	ds_read_b128 v[30:33], v38 offset:7168
	s_waitcnt lgkmcnt(0)
	s_barrier
	s_mov_b32 m0, s35
	s_nop 0
	global_load_lds_dwordx4 v34, s[16:17] nt
	global_load_lds_dwordx4 v34, s[16:17] offset:1024 nt
	global_load_lds_dwordx4 v34, s[16:17] offset:2048 nt
	global_load_lds_dwordx4 v35, s[16:17] offset:3072 nt
	s_add_u32 s16, s16, 0xfa0000
	s_addc_u32 s17, s17, 0
	v_cndmask_b32_e64 v30, 0, v30, s[18:19]
	v_cndmask_b32_e64 v31, 0, v31, s[18:19]
	v_cndmask_b32_e64 v32, 0, v32, s[18:19]
	v_cndmask_b32_e64 v33, 0, v33, s[18:19]
	v_max3_f32 v41, |v18|, |v19|, |v20|
	v_max3_f32 v42, |v21|, |v22|, |v23|
	v_max3_f32 v43, |v24|, |v25|, |v26|
	v_max3_f32 v44, |v27|, |v28|, |v29|
	v_max3_f32 v48, |v30|, |v31|, |v32|
	v_max3_f32 v41, v41, v42, |v33|
	v_max3_f32 v43, v43, v44, v48
	v_max_f32_e32 v41, v41, v43
	v_pk_add_f32 v[2:3], v[2:3], v[18:19]
	v_pk_add_f32 v[4:5], v[4:5], v[20:21]
	v_max_f32_dpp v41, v41, v41 quad_perm:[1,0,3,2] row_mask:0xf bank_mask:0xf
	v_pk_add_f32 v[6:7], v[6:7], v[22:23]
	v_pk_add_f32 v[8:9], v[8:9], v[24:25]
	v_max_f32_dpp v41, v41, v41 quad_perm:[2,3,0,1] row_mask:0xf bank_mask:0xf
	v_pk_add_f32 v[10:11], v[10:11], v[26:27]
	v_pk_add_f32 v[12:13], v[12:13], v[28:29]
	v_max_f32_dpp v41, v41, v41 row_half_mirror row_mask:0xf bank_mask:0xf
	v_pk_add_f32 v[14:15], v[14:15], v[30:31]
	v_pk_add_f32 v[16:17], v[16:17], v[32:33]
	v_max_f32_dpp v41, v41, v41 row_mirror row_mask:0xf bank_mask:0xf
	s_nop 1
	v_max_f32_dpp v41, v41, v41 row_bcast:15 row_mask:0xa bank_mask:0xf
	s_nop 1
	v_max_f32_dpp v41, v41, v41 row_bcast:31 row_mask:0xc bank_mask:0xf
	s_nop 1
	v_readlane_b32 s28, v41, 63
	s_nop 1
	v_div_scale_f32 v48, s[30:31], s28, s28, v47
	v_rcp_f32_e32 v49, v48
	s_nop 0
	v_fma_f32 v50, -v48, v49, 1.0
	v_fmac_f32_e32 v49, v50, v49
	v_mov_b32_e32 v50, s28
	v_div_scale_f32 v50, vcc, s32, v50, s32
	v_mul_f32_e32 v51, v50, v49
	v_fma_f32 v52, -v48, v51, v50
	v_fmac_f32_e32 v51, v52, v49
	v_fma_f32 v48, -v48, v51, v50
	v_div_fmas_f32 v48, v48, v49, v51
	v_div_fixup_f32 v48, v48, s28, v47
	v_cmp_gt_f32_e64 vcc, s28, 0
	v_writelane_b32 v40, s28, 17
	s_nop 0
	v_cndmask_b32_e32 v48, 0, v48, vcc
	v_fmaak_f32 v49, v18, v48, 0x4b400000
	v_fmaak_f32 v50, v19, v48, 0x4b400000
	v_fmaak_f32 v51, v20, v48, 0x4b400000
	v_fmaak_f32 v52, v21, v48, 0x4b400000
	v_perm_b32 v49, v50, v49, s33
	v_perm_b32 v51, v52, v51, s34
	v_or_b32_e32 v124, v49, v51
	v_fmaak_f32 v41, v22, v48, 0x4b400000
	v_fmaak_f32 v42, v23, v48, 0x4b400000
	v_fmaak_f32 v43, v24, v48, 0x4b400000
	v_fmaak_f32 v44, v25, v48, 0x4b400000
	v_perm_b32 v41, v42, v41, s33
	v_perm_b32 v43, v44, v43, s34
	v_or_b32_e32 v125, v41, v43
	v_fmaak_f32 v49, v26, v48, 0x4b400000
	v_fmaak_f32 v50, v27, v48, 0x4b400000
	v_fmaak_f32 v51, v28, v48, 0x4b400000
	v_fmaak_f32 v52, v29, v48, 0x4b400000
	v_perm_b32 v49, v50, v49, s33
	v_perm_b32 v51, v52, v51, s34
	v_or_b32_e32 v126, v49, v51
	v_fmaak_f32 v41, v30, v48, 0x4b400000
	v_fmaak_f32 v42, v31, v48, 0x4b400000
	v_fmaak_f32 v43, v32, v48, 0x4b400000
	v_fmaak_f32 v44, v33, v48, 0x4b400000
	v_perm_b32 v41, v42, v41, s33
	v_perm_b32 v43, v44, v43, s34
	v_or_b32_e32 v127, v41, v43
	s_waitcnt vmcnt(0)
	ds_read_b128 v[18:21], v38 offset:0
	ds_read_b128 v[22:25], v38 offset:1024
	ds_read_b128 v[26:29], v38 offset:2048
	ds_read_b128 v[30:33], v38 offset:3072
	s_waitcnt lgkmcnt(0)
	s_barrier
	s_mov_b32 m0, s36
	s_nop 0
	global_load_lds_dwordx4 v34, s[16:17] nt
	global_load_lds_dwordx4 v34, s[16:17] offset:1024 nt
	global_load_lds_dwordx4 v34, s[16:17] offset:2048 nt
	global_load_lds_dwordx4 v35, s[16:17] offset:3072 nt
	s_add_u32 s16, s16, 0xfa0000
	s_addc_u32 s17, s17, 0
	v_cndmask_b32_e64 v30, 0, v30, s[18:19]
	v_cndmask_b32_e64 v31, 0, v31, s[18:19]
	v_cndmask_b32_e64 v32, 0, v32, s[18:19]
	v_cndmask_b32_e64 v33, 0, v33, s[18:19]
	v_max3_f32 v41, |v18|, |v19|, |v20|
	v_max3_f32 v42, |v21|, |v22|, |v23|
	v_max3_f32 v43, |v24|, |v25|, |v26|
	v_max3_f32 v44, |v27|, |v28|, |v29|
	v_max3_f32 v48, |v30|, |v31|, |v32|
	v_max3_f32 v41, v41, v42, |v33|
	v_max3_f32 v43, v43, v44, v48
	v_max_f32_e32 v41, v41, v43
	v_pk_add_f32 v[2:3], v[2:3], v[18:19]
	v_pk_add_f32 v[4:5], v[4:5], v[20:21]
	v_max_f32_dpp v41, v41, v41 quad_perm:[1,0,3,2] row_mask:0xf bank_mask:0xf
	v_pk_add_f32 v[6:7], v[6:7], v[22:23]
	v_pk_add_f32 v[8:9], v[8:9], v[24:25]
	v_max_f32_dpp v41, v41, v41 quad_perm:[2,3,0,1] row_mask:0xf bank_mask:0xf
	v_pk_add_f32 v[10:11], v[10:11], v[26:27]
	v_pk_add_f32 v[12:13], v[12:13], v[28:29]
	v_max_f32_dpp v41, v41, v41 row_half_mirror row_mask:0xf bank_mask:0xf
	v_pk_add_f32 v[14:15], v[14:15], v[30:31]
	v_pk_add_f32 v[16:17], v[16:17], v[32:33]
	v_max_f32_dpp v41, v41, v41 row_mirror row_mask:0xf bank_mask:0xf
	s_nop 1
	v_max_f32_dpp v41, v41, v41 row_bcast:15 row_mask:0xa bank_mask:0xf
	s_nop 1
	v_max_f32_dpp v41, v41, v41 row_bcast:31 row_mask:0xc bank_mask:0xf
	s_nop 1
	v_readlane_b32 s28, v41, 63
	s_nop 1
	v_div_scale_f32 v48, s[30:31], s28, s28, v47
	v_rcp_f32_e32 v49, v48
	s_nop 0
	v_fma_f32 v50, -v48, v49, 1.0
	v_fmac_f32_e32 v49, v50, v49
	v_mov_b32_e32 v50, s28
	v_div_scale_f32 v50, vcc, s32, v50, s32
	v_mul_f32_e32 v51, v50, v49
	v_fma_f32 v52, -v48, v51, v50
	v_fmac_f32_e32 v51, v52, v49
	v_fma_f32 v48, -v48, v51, v50
	v_div_fmas_f32 v48, v48, v49, v51
	v_div_fixup_f32 v48, v48, s28, v47
	v_cmp_gt_f32_e64 vcc, s28, 0
	v_writelane_b32 v40, s28, 18
	s_nop 0
	v_cndmask_b32_e32 v48, 0, v48, vcc
	v_fmaak_f32 v49, v18, v48, 0x4b400000
	v_fmaak_f32 v50, v19, v48, 0x4b400000
	v_fmaak_f32 v51, v20, v48, 0x4b400000
	v_fmaak_f32 v52, v21, v48, 0x4b400000
	v_perm_b32 v49, v50, v49, s33
	v_perm_b32 v51, v52, v51, s34
	v_or_b32_e32 v36, v49, v51
	v_fmaak_f32 v41, v22, v48, 0x4b400000
	v_fmaak_f32 v42, v23, v48, 0x4b400000
	v_fmaak_f32 v43, v24, v48, 0x4b400000
	v_fmaak_f32 v44, v25, v48, 0x4b400000
	v_perm_b32 v41, v42, v41, s33
	v_perm_b32 v43, v44, v43, s34
	v_or_b32_e32 v37, v41, v43
	v_fmaak_f32 v49, v26, v48, 0x4b400000
	v_fmaak_f32 v50, v27, v48, 0x4b400000
	v_fmaak_f32 v51, v28, v48, 0x4b400000
	v_fmaak_f32 v52, v29, v48, 0x4b400000
	v_perm_b32 v49, v50, v49, s33
	v_perm_b32 v51, v52, v51, s34
	v_or_b32_e32 v45, v49, v51
	v_fmaak_f32 v41, v30, v48, 0x4b400000
	v_fmaak_f32 v42, v31, v48, 0x4b400000
	v_fmaak_f32 v43, v32, v48, 0x4b400000
	v_fmaak_f32 v44, v33, v48, 0x4b400000
	v_perm_b32 v41, v42, v41, s33
	v_perm_b32 v43, v44, v43, s34
	v_or_b32_e32 v46, v41, v43
	s_waitcnt vmcnt(0)
	ds_read_b128 v[18:21], v38 offset:4096
	ds_read_b128 v[22:25], v38 offset:5120
	ds_read_b128 v[26:29], v38 offset:6144
	ds_read_b128 v[30:33], v38 offset:7168
	s_waitcnt lgkmcnt(0)
	s_barrier
	s_mov_b32 m0, s35
	s_nop 0
	global_load_lds_dwordx4 v34, s[16:17] nt
	global_load_lds_dwordx4 v34, s[16:17] offset:1024 nt
	global_load_lds_dwordx4 v34, s[16:17] offset:2048 nt
	global_load_lds_dwordx4 v35, s[16:17] offset:3072 nt
	s_add_u32 s16, s16, 0xfa0000
	s_addc_u32 s17, s17, 0
	v_cndmask_b32_e64 v30, 0, v30, s[18:19]
	v_cndmask_b32_e64 v31, 0, v31, s[18:19]
	v_cndmask_b32_e64 v32, 0, v32, s[18:19]
	v_cndmask_b32_e64 v33, 0, v33, s[18:19]
	v_max3_f32 v41, |v18|, |v19|, |v20|
	v_max3_f32 v42, |v21|, |v22|, |v23|
	v_max3_f32 v43, |v24|, |v25|, |v26|
	v_max3_f32 v44, |v27|, |v28|, |v29|
	v_max3_f32 v48, |v30|, |v31|, |v32|
	v_max3_f32 v41, v41, v42, |v33|
	v_max3_f32 v43, v43, v44, v48
	v_max_f32_e32 v41, v41, v43
	v_pk_add_f32 v[2:3], v[2:3], v[18:19]
	v_pk_add_f32 v[4:5], v[4:5], v[20:21]
	v_max_f32_dpp v41, v41, v41 quad_perm:[1,0,3,2] row_mask:0xf bank_mask:0xf
	v_pk_add_f32 v[6:7], v[6:7], v[22:23]
	v_pk_add_f32 v[8:9], v[8:9], v[24:25]
	v_max_f32_dpp v41, v41, v41 quad_perm:[2,3,0,1] row_mask:0xf bank_mask:0xf
	v_pk_add_f32 v[10:11], v[10:11], v[26:27]
	v_pk_add_f32 v[12:13], v[12:13], v[28:29]
	v_max_f32_dpp v41, v41, v41 row_half_mirror row_mask:0xf bank_mask:0xf
	v_pk_add_f32 v[14:15], v[14:15], v[30:31]
	v_pk_add_f32 v[16:17], v[16:17], v[32:33]
	v_max_f32_dpp v41, v41, v41 row_mirror row_mask:0xf bank_mask:0xf
	s_nop 1
	v_max_f32_dpp v41, v41, v41 row_bcast:15 row_mask:0xa bank_mask:0xf
	s_nop 1
	v_max_f32_dpp v41, v41, v41 row_bcast:31 row_mask:0xc bank_mask:0xf
	s_nop 1
	v_readlane_b32 s28, v41, 63
	s_nop 1
	v_div_scale_f32 v48, s[30:31], s28, s28, v47
	v_rcp_f32_e32 v49, v48
	s_nop 0
	v_fma_f32 v50, -v48, v49, 1.0
	v_fmac_f32_e32 v49, v50, v49
	v_mov_b32_e32 v50, s28
	v_div_scale_f32 v50, vcc, s32, v50, s32
	v_mul_f32_e32 v51, v50, v49
	v_fma_f32 v52, -v48, v51, v50
	v_fmac_f32_e32 v51, v52, v49
	v_fma_f32 v48, -v48, v51, v50
	v_div_fmas_f32 v48, v48, v49, v51
	v_div_fixup_f32 v48, v48, s28, v47
	v_cmp_gt_f32_e64 vcc, s28, 0
	v_writelane_b32 v40, s28, 19
	s_nop 0
	v_cndmask_b32_e32 v48, 0, v48, vcc
	v_fmaak_f32 v49, v18, v48, 0x4b400000
	v_fmaak_f32 v50, v19, v48, 0x4b400000
	v_fmaak_f32 v51, v20, v48, 0x4b400000
	v_fmaak_f32 v52, v21, v48, 0x4b400000
	v_perm_b32 v49, v50, v49, s33
	v_perm_b32 v51, v52, v51, s34
	v_or_b32_e32 v53, v49, v51
	v_fmaak_f32 v41, v22, v48, 0x4b400000
	v_fmaak_f32 v42, v23, v48, 0x4b400000
	v_fmaak_f32 v43, v24, v48, 0x4b400000
	v_fmaak_f32 v44, v25, v48, 0x4b400000
	v_perm_b32 v41, v42, v41, s33
	v_perm_b32 v43, v44, v43, s34
	v_or_b32_e32 v54, v41, v43
	v_fmaak_f32 v49, v26, v48, 0x4b400000
	v_fmaak_f32 v50, v27, v48, 0x4b400000
	v_fmaak_f32 v51, v28, v48, 0x4b400000
	v_fmaak_f32 v52, v29, v48, 0x4b400000
	v_perm_b32 v49, v50, v49, s33
	v_perm_b32 v51, v52, v51, s34
	v_or_b32_e32 v55, v49, v51
	v_fmaak_f32 v41, v30, v48, 0x4b400000
	v_fmaak_f32 v42, v31, v48, 0x4b400000
	v_fmaak_f32 v43, v32, v48, 0x4b400000
	v_fmaak_f32 v44, v33, v48, 0x4b400000
	v_perm_b32 v41, v42, v41, s33
	v_perm_b32 v43, v44, v43, s34
	v_or_b32_e32 v1, v41, v43
	s_waitcnt vmcnt(0)
	ds_read_b128 v[18:21], v38 offset:0
	ds_read_b128 v[22:25], v38 offset:1024
	ds_read_b128 v[26:29], v38 offset:2048
	ds_read_b128 v[30:33], v38 offset:3072
	s_waitcnt lgkmcnt(0)
	s_barrier
	s_mov_b32 m0, s36
	s_nop 0
	global_load_lds_dwordx4 v34, s[16:17] nt
	global_load_lds_dwordx4 v34, s[16:17] offset:1024 nt
	global_load_lds_dwordx4 v34, s[16:17] offset:2048 nt
	global_load_lds_dwordx4 v35, s[16:17] offset:3072 nt
	s_add_u32 s16, s16, 0xfa0000
	s_addc_u32 s17, s17, 0
	v_cndmask_b32_e64 v30, 0, v30, s[18:19]
	v_cndmask_b32_e64 v31, 0, v31, s[18:19]
	v_cndmask_b32_e64 v32, 0, v32, s[18:19]
	v_cndmask_b32_e64 v33, 0, v33, s[18:19]
	v_max3_f32 v41, |v18|, |v19|, |v20|
	v_max3_f32 v42, |v21|, |v22|, |v23|
	v_max3_f32 v43, |v24|, |v25|, |v26|
	v_max3_f32 v44, |v27|, |v28|, |v29|
	v_max3_f32 v48, |v30|, |v31|, |v32|
	v_max3_f32 v41, v41, v42, |v33|
	v_max3_f32 v43, v43, v44, v48
	v_max_f32_e32 v41, v41, v43
	v_pk_add_f32 v[2:3], v[2:3], v[18:19]
	v_pk_add_f32 v[4:5], v[4:5], v[20:21]
	v_max_f32_dpp v41, v41, v41 quad_perm:[1,0,3,2] row_mask:0xf bank_mask:0xf
	v_pk_add_f32 v[6:7], v[6:7], v[22:23]
	v_pk_add_f32 v[8:9], v[8:9], v[24:25]
	v_max_f32_dpp v41, v41, v41 quad_perm:[2,3,0,1] row_mask:0xf bank_mask:0xf
	v_pk_add_f32 v[10:11], v[10:11], v[26:27]
	v_pk_add_f32 v[12:13], v[12:13], v[28:29]
	v_max_f32_dpp v41, v41, v41 row_half_mirror row_mask:0xf bank_mask:0xf
	v_pk_add_f32 v[14:15], v[14:15], v[30:31]
	v_pk_add_f32 v[16:17], v[16:17], v[32:33]
	v_max_f32_dpp v41, v41, v41 row_mirror row_mask:0xf bank_mask:0xf
	s_nop 1
	v_max_f32_dpp v41, v41, v41 row_bcast:15 row_mask:0xa bank_mask:0xf
	s_nop 1
	v_max_f32_dpp v41, v41, v41 row_bcast:31 row_mask:0xc bank_mask:0xf
	s_nop 1
	v_readlane_b32 s28, v41, 63
	s_nop 1
	v_div_scale_f32 v48, s[30:31], s28, s28, v47
	v_rcp_f32_e32 v49, v48
	s_nop 0
	v_fma_f32 v50, -v48, v49, 1.0
	v_fmac_f32_e32 v49, v50, v49
	v_mov_b32_e32 v50, s28
	v_div_scale_f32 v50, vcc, s32, v50, s32
	v_mul_f32_e32 v51, v50, v49
	v_fma_f32 v52, -v48, v51, v50
	v_fmac_f32_e32 v51, v52, v49
	v_fma_f32 v48, -v48, v51, v50
	v_div_fmas_f32 v48, v48, v49, v51
	v_div_fixup_f32 v48, v48, s28, v47
	v_cmp_gt_f32_e64 vcc, s28, 0
	v_writelane_b32 v40, s28, 20
	s_nop 0
	v_cndmask_b32_e32 v48, 0, v48, vcc
	v_fmaak_f32 v49, v18, v48, 0x4b400000
	v_fmaak_f32 v50, v19, v48, 0x4b400000
	v_fmaak_f32 v51, v20, v48, 0x4b400000
	v_fmaak_f32 v52, v21, v48, 0x4b400000
	v_perm_b32 v49, v50, v49, s33
	v_perm_b32 v51, v52, v51, s34
	v_or_b32_e32 v49, v49, v51
	s_add_u32 s20, s20, 0xa00000
	s_addc_u32 s21, s21, 0
	s_add_u32 s22, s22, 0xa00000
	s_addc_u32 s23, s23, 0
	s_add_u32 s24, s24, 0xa00000
	s_addc_u32 s25, s25, 0
	s_add_u32 s26, s26, 0xa00000
	s_addc_u32 s27, s27, 0
	global_store_dword v39, v49, s[20:21]
	v_fmaak_f32 v41, v22, v48, 0x4b400000
	v_fmaak_f32 v42, v23, v48, 0x4b400000
	v_fmaak_f32 v43, v24, v48, 0x4b400000
	v_fmaak_f32 v44, v25, v48, 0x4b400000
	v_perm_b32 v41, v42, v41, s33
	v_perm_b32 v43, v44, v43, s34
	v_or_b32_e32 v41, v41, v43
	global_store_dword v39, v41, s[22:23]
	v_fmaak_f32 v49, v26, v48, 0x4b400000
	v_fmaak_f32 v50, v27, v48, 0x4b400000
	v_fmaak_f32 v51, v28, v48, 0x4b400000
	v_fmaak_f32 v52, v29, v48, 0x4b400000
	v_perm_b32 v49, v50, v49, s33
	v_perm_b32 v51, v52, v51, s34
	v_or_b32_e32 v49, v49, v51
	global_store_dword v39, v49, s[24:25]
	v_fmaak_f32 v41, v30, v48, 0x4b400000
	v_fmaak_f32 v42, v31, v48, 0x4b400000
	v_fmaak_f32 v43, v32, v48, 0x4b400000
	v_fmaak_f32 v44, v33, v48, 0x4b400000
	v_perm_b32 v41, v42, v41, s33
	v_perm_b32 v43, v44, v43, s34
	v_or_b32_e32 v41, v41, v43
	global_store_dword v39, v41, s[26:27]
	s_waitcnt vmcnt(4)
	ds_read_b128 v[18:21], v38 offset:4096
	ds_read_b128 v[22:25], v38 offset:5120
	ds_read_b128 v[26:29], v38 offset:6144
	ds_read_b128 v[30:33], v38 offset:7168
	s_waitcnt lgkmcnt(0)
	s_barrier
	s_mov_b32 m0, s35
	s_nop 0
	global_load_lds_dwordx4 v34, s[16:17] nt
	global_load_lds_dwordx4 v34, s[16:17] offset:1024 nt
	global_load_lds_dwordx4 v34, s[16:17] offset:2048 nt
	global_load_lds_dwordx4 v35, s[16:17] offset:3072 nt
	s_add_u32 s16, s16, 0xfa0000
	s_addc_u32 s17, s17, 0
	v_cndmask_b32_e64 v30, 0, v30, s[18:19]
	v_cndmask_b32_e64 v31, 0, v31, s[18:19]
	v_cndmask_b32_e64 v32, 0, v32, s[18:19]
	v_cndmask_b32_e64 v33, 0, v33, s[18:19]
	v_max3_f32 v41, |v18|, |v19|, |v20|
	v_max3_f32 v42, |v21|, |v22|, |v23|
	v_max3_f32 v43, |v24|, |v25|, |v26|
	v_max3_f32 v44, |v27|, |v28|, |v29|
	v_max3_f32 v48, |v30|, |v31|, |v32|
	v_max3_f32 v41, v41, v42, |v33|
	v_max3_f32 v43, v43, v44, v48
	v_max_f32_e32 v41, v41, v43
	v_pk_add_f32 v[2:3], v[2:3], v[18:19]
	v_pk_add_f32 v[4:5], v[4:5], v[20:21]
	v_max_f32_dpp v41, v41, v41 quad_perm:[1,0,3,2] row_mask:0xf bank_mask:0xf
	v_pk_add_f32 v[6:7], v[6:7], v[22:23]
	v_pk_add_f32 v[8:9], v[8:9], v[24:25]
	v_max_f32_dpp v41, v41, v41 quad_perm:[2,3,0,1] row_mask:0xf bank_mask:0xf
	v_pk_add_f32 v[10:11], v[10:11], v[26:27]
	v_pk_add_f32 v[12:13], v[12:13], v[28:29]
	v_max_f32_dpp v41, v41, v41 row_half_mirror row_mask:0xf bank_mask:0xf
	v_pk_add_f32 v[14:15], v[14:15], v[30:31]
	v_pk_add_f32 v[16:17], v[16:17], v[32:33]
	v_max_f32_dpp v41, v41, v41 row_mirror row_mask:0xf bank_mask:0xf
	s_nop 1
	v_max_f32_dpp v41, v41, v41 row_bcast:15 row_mask:0xa bank_mask:0xf
	s_nop 1
	v_max_f32_dpp v41, v41, v41 row_bcast:31 row_mask:0xc bank_mask:0xf
	s_nop 1
	v_readlane_b32 s28, v41, 63
	s_nop 1
	v_div_scale_f32 v48, s[30:31], s28, s28, v47
	v_rcp_f32_e32 v49, v48
	s_nop 0
	v_fma_f32 v50, -v48, v49, 1.0
	v_fmac_f32_e32 v49, v50, v49
	v_mov_b32_e32 v50, s28
	v_div_scale_f32 v50, vcc, s32, v50, s32
	v_mul_f32_e32 v51, v50, v49
	v_fma_f32 v52, -v48, v51, v50
	v_fmac_f32_e32 v51, v52, v49
	v_fma_f32 v48, -v48, v51, v50
	v_div_fmas_f32 v48, v48, v49, v51
	v_div_fixup_f32 v48, v48, s28, v47
	v_cmp_gt_f32_e64 vcc, s28, 0
	v_writelane_b32 v40, s28, 21
	s_nop 0
	v_cndmask_b32_e32 v48, 0, v48, vcc
	v_fmaak_f32 v49, v18, v48, 0x4b400000
	v_fmaak_f32 v50, v19, v48, 0x4b400000
	v_fmaak_f32 v51, v20, v48, 0x4b400000
	v_fmaak_f32 v52, v21, v48, 0x4b400000
	v_perm_b32 v49, v50, v49, s33
	v_perm_b32 v51, v52, v51, s34
	v_or_b32_e32 v49, v49, v51
	s_add_u32 s20, s20, 0x80000
	s_addc_u32 s21, s21, 0
	s_add_u32 s22, s22, 0x80000
	s_addc_u32 s23, s23, 0
	s_add_u32 s24, s24, 0x80000
	s_addc_u32 s25, s25, 0
	s_add_u32 s26, s26, 0x80000
	s_addc_u32 s27, s27, 0
	global_store_dword v39, v49, s[20:21]
	v_fmaak_f32 v41, v22, v48, 0x4b400000
	v_fmaak_f32 v42, v23, v48, 0x4b400000
	v_fmaak_f32 v43, v24, v48, 0x4b400000
	v_fmaak_f32 v44, v25, v48, 0x4b400000
	v_perm_b32 v41, v42, v41, s33
	v_perm_b32 v43, v44, v43, s34
	v_or_b32_e32 v41, v41, v43
	global_store_dword v39, v41, s[22:23]
	v_fmaak_f32 v49, v26, v48, 0x4b400000
	v_fmaak_f32 v50, v27, v48, 0x4b400000
	v_fmaak_f32 v51, v28, v48, 0x4b400000
	v_fmaak_f32 v52, v29, v48, 0x4b400000
	v_perm_b32 v49, v50, v49, s33
	v_perm_b32 v51, v52, v51, s34
	v_or_b32_e32 v49, v49, v51
	global_store_dword v39, v49, s[24:25]
	v_fmaak_f32 v41, v30, v48, 0x4b400000
	v_fmaak_f32 v42, v31, v48, 0x4b400000
	v_fmaak_f32 v43, v32, v48, 0x4b400000
	v_fmaak_f32 v44, v33, v48, 0x4b400000
	v_perm_b32 v41, v42, v41, s33
	v_perm_b32 v43, v44, v43, s34
	v_or_b32_e32 v41, v41, v43
	global_store_dword v39, v41, s[26:27]
	s_waitcnt vmcnt(4)
	ds_read_b128 v[18:21], v38 offset:0
	ds_read_b128 v[22:25], v38 offset:1024
	ds_read_b128 v[26:29], v38 offset:2048
	ds_read_b128 v[30:33], v38 offset:3072
	s_waitcnt lgkmcnt(0)
	s_barrier
	s_mov_b32 m0, s36
	s_nop 0
	global_load_lds_dwordx4 v34, s[16:17] nt
	global_load_lds_dwordx4 v34, s[16:17] offset:1024 nt
	global_load_lds_dwordx4 v34, s[16:17] offset:2048 nt
	global_load_lds_dwordx4 v35, s[16:17] offset:3072 nt
	s_add_u32 s16, s16, 0xfa0000
	s_addc_u32 s17, s17, 0
	v_cndmask_b32_e64 v30, 0, v30, s[18:19]
	v_cndmask_b32_e64 v31, 0, v31, s[18:19]
	v_cndmask_b32_e64 v32, 0, v32, s[18:19]
	v_cndmask_b32_e64 v33, 0, v33, s[18:19]
	v_max3_f32 v41, |v18|, |v19|, |v20|
	v_max3_f32 v42, |v21|, |v22|, |v23|
	v_max3_f32 v43, |v24|, |v25|, |v26|
	v_max3_f32 v44, |v27|, |v28|, |v29|
	v_max3_f32 v48, |v30|, |v31|, |v32|
	v_max3_f32 v41, v41, v42, |v33|
	v_max3_f32 v43, v43, v44, v48
	v_max_f32_e32 v41, v41, v43
	v_pk_add_f32 v[2:3], v[2:3], v[18:19]
	v_pk_add_f32 v[4:5], v[4:5], v[20:21]
	v_max_f32_dpp v41, v41, v41 quad_perm:[1,0,3,2] row_mask:0xf bank_mask:0xf
	v_pk_add_f32 v[6:7], v[6:7], v[22:23]
	v_pk_add_f32 v[8:9], v[8:9], v[24:25]
	v_max_f32_dpp v41, v41, v41 quad_perm:[2,3,0,1] row_mask:0xf bank_mask:0xf
	v_pk_add_f32 v[10:11], v[10:11], v[26:27]
	v_pk_add_f32 v[12:13], v[12:13], v[28:29]
	v_max_f32_dpp v41, v41, v41 row_half_mirror row_mask:0xf bank_mask:0xf
	v_pk_add_f32 v[14:15], v[14:15], v[30:31]
	v_pk_add_f32 v[16:17], v[16:17], v[32:33]
	v_max_f32_dpp v41, v41, v41 row_mirror row_mask:0xf bank_mask:0xf
	s_nop 1
	v_max_f32_dpp v41, v41, v41 row_bcast:15 row_mask:0xa bank_mask:0xf
	s_nop 1
	v_max_f32_dpp v41, v41, v41 row_bcast:31 row_mask:0xc bank_mask:0xf
	s_nop 1
	v_readlane_b32 s28, v41, 63
	s_nop 1
	v_div_scale_f32 v48, s[30:31], s28, s28, v47
	v_rcp_f32_e32 v49, v48
	s_nop 0
	v_fma_f32 v50, -v48, v49, 1.0
	v_fmac_f32_e32 v49, v50, v49
	v_mov_b32_e32 v50, s28
	v_div_scale_f32 v50, vcc, s32, v50, s32
	v_mul_f32_e32 v51, v50, v49
	v_fma_f32 v52, -v48, v51, v50
	v_fmac_f32_e32 v51, v52, v49
	v_fma_f32 v48, -v48, v51, v50
	v_div_fmas_f32 v48, v48, v49, v51
	v_div_fixup_f32 v48, v48, s28, v47
	v_cmp_gt_f32_e64 vcc, s28, 0
	v_writelane_b32 v40, s28, 22
	s_nop 0
	v_cndmask_b32_e32 v48, 0, v48, vcc
	v_fmaak_f32 v49, v18, v48, 0x4b400000
	v_fmaak_f32 v50, v19, v48, 0x4b400000
	v_fmaak_f32 v51, v20, v48, 0x4b400000
	v_fmaak_f32 v52, v21, v48, 0x4b400000
	v_perm_b32 v49, v50, v49, s33
	v_perm_b32 v51, v52, v51, s34
	v_or_b32_e32 v49, v49, v51
	s_add_u32 s20, s20, 0x80000
	s_addc_u32 s21, s21, 0
	s_add_u32 s22, s22, 0x80000
	s_addc_u32 s23, s23, 0
	s_add_u32 s24, s24, 0x80000
	s_addc_u32 s25, s25, 0
	s_add_u32 s26, s26, 0x80000
	s_addc_u32 s27, s27, 0
	global_store_dword v39, v49, s[20:21]
	v_fmaak_f32 v41, v22, v48, 0x4b400000
	v_fmaak_f32 v42, v23, v48, 0x4b400000
	v_fmaak_f32 v43, v24, v48, 0x4b400000
	v_fmaak_f32 v44, v25, v48, 0x4b400000
	v_perm_b32 v41, v42, v41, s33
	v_perm_b32 v43, v44, v43, s34
	v_or_b32_e32 v41, v41, v43
	global_store_dword v39, v41, s[22:23]
	v_fmaak_f32 v49, v26, v48, 0x4b400000
	v_fmaak_f32 v50, v27, v48, 0x4b400000
	v_fmaak_f32 v51, v28, v48, 0x4b400000
	v_fmaak_f32 v52, v29, v48, 0x4b400000
	v_perm_b32 v49, v50, v49, s33
	v_perm_b32 v51, v52, v51, s34
	v_or_b32_e32 v49, v49, v51
	global_store_dword v39, v49, s[24:25]
	v_fmaak_f32 v41, v30, v48, 0x4b400000
	v_fmaak_f32 v42, v31, v48, 0x4b400000
	v_fmaak_f32 v43, v32, v48, 0x4b400000
	v_fmaak_f32 v44, v33, v48, 0x4b400000
	v_perm_b32 v41, v42, v41, s33
	v_perm_b32 v43, v44, v43, s34
	v_or_b32_e32 v41, v41, v43
	global_store_dword v39, v41, s[26:27]
	s_waitcnt vmcnt(4)
	ds_read_b128 v[18:21], v38 offset:4096
	ds_read_b128 v[22:25], v38 offset:5120
	ds_read_b128 v[26:29], v38 offset:6144
	ds_read_b128 v[30:33], v38 offset:7168
	s_waitcnt lgkmcnt(0)
	s_cmp_eq_u32 s29, 1
	s_cbranch_scc0 .Lk1_nodma24
	s_mov_b32 m0, s35
	s_nop 0
	global_load_lds_dwordx4 v34, s[16:17] nt
	global_load_lds_dwordx4 v34, s[16:17] offset:1024 nt
	global_load_lds_dwordx4 v34, s[16:17] offset:2048 nt
	global_load_lds_dwordx4 v35, s[16:17] offset:3072 nt
	s_add_u32 s16, s16, 0xfa0000
	s_addc_u32 s17, s17, 0

.Lk1_flush:
	s_add_u32 s20, s40, 0x0
	s_addc_u32 s21, s41, 0
	s_add_u32 s22, s20, 0x186a000
	s_addc_u32 s23, s21, 0
	s_add_u32 s24, s22, 0x186a000
	s_addc_u32 s25, s23, 0
	s_add_u32 s26, s24, 0x186a000
	s_addc_u32 s27, s25, 0
	global_store_dword v39, v56, s[20:21] sc1
	global_store_dword v39, v57, s[22:23] sc1
	global_store_dword v39, v58, s[24:25] sc1
	global_store_dword v39, v59, s[26:27] sc1
	s_add_u32 s20, s20, 0x80000
	s_addc_u32 s21, s21, 0
	s_add_u32 s22, s22, 0x80000
	s_addc_u32 s23, s23, 0
	s_add_u32 s24, s24, 0x80000
	s_addc_u32 s25, s25, 0
	s_add_u32 s26, s26, 0x80000
	s_addc_u32 s27, s27, 0
	global_store_dword v39, v60, s[20:21] sc1
	global_store_dword v39, v61, s[22:23] sc1
	global_store_dword v39, v62, s[24:25] sc1
	global_store_dword v39, v63, s[26:27] sc1
	s_add_u32 s20, s20, 0x80000
	s_addc_u32 s21, s21, 0
	s_add_u32 s22, s22, 0x80000
	s_addc_u32 s23, s23, 0
	s_add_u32 s24, s24, 0x80000
	s_addc_u32 s25, s25, 0
	s_add_u32 s26, s26, 0x80000
	s_addc_u32 s27, s27, 0
	global_store_dword v39, v64, s[20:21] sc1
	global_store_dword v39, v65, s[22:23] sc1
	global_store_dword v39, v66, s[24:25] sc1
	global_store_dword v39, v67, s[26:27] sc1
	s_add_u32 s20, s20, 0x80000
	s_addc_u32 s21, s21, 0
	s_add_u32 s22, s22, 0x80000
	s_addc_u32 s23, s23, 0
	s_add_u32 s24, s24, 0x80000
	s_addc_u32 s25, s25, 0
	s_add_u32 s26, s26, 0x80000
	s_addc_u32 s27, s27, 0
	global_store_dword v39, v68, s[20:21] sc1
	global_store_dword v39, v69, s[22:23] sc1
	global_store_dword v39, v70, s[24:25] sc1
	global_store_dword v39, v71, s[26:27] sc1
	s_add_u32 s20, s20, 0x80000
	s_addc_u32 s21, s21, 0
	s_add_u32 s22, s22, 0x80000
	s_addc_u32 s23, s23, 0
	s_add_u32 s24, s24, 0x80000
	s_addc_u32 s25, s25, 0
	s_add_u32 s26, s26, 0x80000
	s_addc_u32 s27, s27, 0
	global_store_dword v39, v72, s[20:21] sc1
	global_store_dword v39, v73, s[22:23] sc1
	global_store_dword v39, v74, s[24:25] sc1
	global_store_dword v39, v75, s[26:27] sc1
	s_add_u32 s20, s20, 0x80000
	s_addc_u32 s21, s21, 0
	s_add_u32 s22, s22, 0x80000
	s_addc_u32 s23, s23, 0
	s_add_u32 s24, s24, 0x80000
	s_addc_u32 s25, s25, 0
	s_add_u32 s26, s26, 0x80000
	s_addc_u32 s27, s27, 0
	global_store_dword v39, v76, s[20:21] sc1
	global_store_dword v39, v77, s[22:23] sc1
	global_store_dword v39, v78, s[24:25] sc1
	global_store_dword v39, v79, s[26:27] sc1
	s_add_u32 s20, s20, 0x80000
	s_addc_u32 s21, s21, 0
	s_add_u32 s22, s22, 0x80000
	s_addc_u32 s23, s23, 0
	s_add_u32 s24, s24, 0x80000
	s_addc_u32 s25, s25, 0
	s_add_u32 s26, s26, 0x80000
	s_addc_u32 s27, s27, 0
	global_store_dword v39, v80, s[20:21] sc1
	global_store_dword v39, v81, s[22:23] sc1
	global_store_dword v39, v82, s[24:25] sc1
	global_store_dword v39, v83, s[26:27] sc1
	s_add_u32 s20, s20, 0x80000
	s_addc_u32 s21, s21, 0
	s_add_u32 s22, s22, 0x80000
	s_addc_u32 s23, s23, 0
	s_add_u32 s24, s24, 0x80000
	s_addc_u32 s25, s25, 0
	s_add_u32 s26, s26, 0x80000
	s_addc_u32 s27, s27, 0
	global_store_dword v39, v84, s[20:21] sc1
	global_store_dword v39, v85, s[22:23] sc1
	global_store_dword v39, v86, s[24:25] sc1
	global_store_dword v39, v87, s[26:27] sc1
	s_add_u32 s20, s20, 0x80000
	s_addc_u32 s21, s21, 0
	s_add_u32 s22, s22, 0x80000
	s_addc_u32 s23, s23, 0
	s_add_u32 s24, s24, 0x80000
	s_addc_u32 s25, s25, 0
	s_add_u32 s26, s26, 0x80000
	s_addc_u32 s27, s27, 0
	global_store_dword v39, v88, s[20:21] sc1
	global_store_dword v39, v89, s[22:23] sc1
	global_store_dword v39, v90, s[24:25] sc1
	global_store_dword v39, v91, s[26:27] sc1
	s_add_u32 s20, s20, 0x80000
	s_addc_u32 s21, s21, 0
	s_add_u32 s22, s22, 0x80000
	s_addc_u32 s23, s23, 0
	s_add_u32 s24, s24, 0x80000
	s_addc_u32 s25, s25, 0
	s_add_u32 s26, s26, 0x80000
	s_addc_u32 s27, s27, 0
	global_store_dword v39, v92, s[20:21] sc1
	global_store_dword v39, v93, s[22:23] sc1
	global_store_dword v39, v94, s[24:25] sc1
	global_store_dword v39, v95, s[26:27] sc1
	s_add_u32 s20, s20, 0x80000
	s_addc_u32 s21, s21, 0
	s_add_u32 s22, s22, 0x80000
	s_addc_u32 s23, s23, 0
	s_add_u32 s24, s24, 0x80000
	s_addc_u32 s25, s25, 0
	s_add_u32 s26, s26, 0x80000
	s_addc_u32 s27, s27, 0
	global_store_dword v39, v96, s[20:21] sc1
	global_store_dword v39, v97, s[22:23] sc1
	global_store_dword v39, v98, s[24:25] sc1
	global_store_dword v39, v99, s[26:27] sc1
	s_add_u32 s20, s20, 0x80000
	s_addc_u32 s21, s21, 0
	s_add_u32 s22, s22, 0x80000
	s_addc_u32 s23, s23, 0
	s_add_u32 s24, s24, 0x80000
	s_addc_u32 s25, s25, 0
	s_add_u32 s26, s26, 0x80000
	s_addc_u32 s27, s27, 0
	global_store_dword v39, v100, s[20:21] sc1
	global_store_dword v39, v101, s[22:23] sc1
	global_store_dword v39, v102, s[24:25] sc1
	global_store_dword v39, v103, s[26:27] sc1
	s_add_u32 s20, s20, 0x80000
	s_addc_u32 s21, s21, 0
	s_add_u32 s22, s22, 0x80000
	s_addc_u32 s23, s23, 0
	s_add_u32 s24, s24, 0x80000
	s_addc_u32 s25, s25, 0
	s_add_u32 s26, s26, 0x80000
	s_addc_u32 s27, s27, 0
	global_store_dword v39, v104, s[20:21] sc1
	global_store_dword v39, v105, s[22:23] sc1
	global_store_dword v39, v106, s[24:25] sc1
	global_store_dword v39, v107, s[26:27] sc1
	s_add_u32 s20, s20, 0x80000
	s_addc_u32 s21, s21, 0
	s_add_u32 s22, s22, 0x80000
	s_addc_u32 s23, s23, 0
	s_add_u32 s24, s24, 0x80000
	s_addc_u32 s25, s25, 0
	s_add_u32 s26, s26, 0x80000
	s_addc_u32 s27, s27, 0
	global_store_dword v39, v108, s[20:21] sc1
	global_store_dword v39, v109, s[22:23] sc1
	global_store_dword v39, v110, s[24:25] sc1
	global_store_dword v39, v111, s[26:27] sc1
	s_add_u32 s20, s20, 0x80000
	s_addc_u32 s21, s21, 0
	s_add_u32 s22, s22, 0x80000
	s_addc_u32 s23, s23, 0
	s_add_u32 s24, s24, 0x80000
	s_addc_u32 s25, s25, 0
	s_add_u32 s26, s26, 0x80000
	s_addc_u32 s27, s27, 0
	global_store_dword v39, v112, s[20:21] sc1
	global_store_dword v39, v113, s[22:23] sc1
	global_store_dword v39, v114, s[24:25] sc1
	global_store_dword v39, v115, s[26:27] sc1
	s_add_u32 s20, s20, 0x80000
	s_addc_u32 s21, s21, 0
	s_add_u32 s22, s22, 0x80000
	s_addc_u32 s23, s23, 0
	s_add_u32 s24, s24, 0x80000
	s_addc_u32 s25, s25, 0
	s_add_u32 s26, s26, 0x80000
	s_addc_u32 s27, s27, 0
	global_store_dword v39, v116, s[20:21] sc1
	global_store_dword v39, v117, s[22:23] sc1
	global_store_dword v39, v118, s[24:25] sc1
	global_store_dword v39, v119, s[26:27] sc1
	s_add_u32 s20, s20, 0x80000
	s_addc_u32 s21, s21, 0
	s_add_u32 s22, s22, 0x80000
	s_addc_u32 s23, s23, 0
	s_add_u32 s24, s24, 0x80000
	s_addc_u32 s25, s25, 0
	s_add_u32 s26, s26, 0x80000
	s_addc_u32 s27, s27, 0
	global_store_dword v39, v120, s[20:21] sc1
	global_store_dword v39, v121, s[22:23] sc1
	global_store_dword v39, v122, s[24:25] sc1
	global_store_dword v39, v123, s[26:27] sc1
	s_add_u32 s20, s20, 0x80000
	s_addc_u32 s21, s21, 0
	s_add_u32 s22, s22, 0x80000
	s_addc_u32 s23, s23, 0
	s_add_u32 s24, s24, 0x80000
	s_addc_u32 s25, s25, 0
	s_add_u32 s26, s26, 0x80000
	s_addc_u32 s27, s27, 0
	global_store_dword v39, v124, s[20:21] sc1
	global_store_dword v39, v125, s[22:23] sc1
	global_store_dword v39, v126, s[24:25] sc1
	global_store_dword v39, v127, s[26:27] sc1
	s_add_u32 s20, s20, 0x80000
	s_addc_u32 s21, s21, 0
	s_add_u32 s22, s22, 0x80000
	s_addc_u32 s23, s23, 0
	s_add_u32 s24, s24, 0x80000
	s_addc_u32 s25, s25, 0
	s_add_u32 s26, s26, 0x80000
	s_addc_u32 s27, s27, 0
	global_store_dword v39, v36, s[20:21] sc1
	global_store_dword v39, v37, s[22:23] sc1
	global_store_dword v39, v45, s[24:25] sc1
	global_store_dword v39, v46, s[26:27] sc1
	s_add_u32 s20, s20, 0x80000
	s_addc_u32 s21, s21, 0
	s_add_u32 s22, s22, 0x80000
	s_addc_u32 s23, s23, 0
	s_add_u32 s24, s24, 0x80000
	s_addc_u32 s25, s25, 0
	s_add_u32 s26, s26, 0x80000
	s_addc_u32 s27, s27, 0
	global_store_dword v39, v53, s[20:21] sc1
	global_store_dword v39, v54, s[22:23] sc1
	global_store_dword v39, v55, s[24:25] sc1
	global_store_dword v39, v1, s[26:27] sc1
	v_mul_f32_e32 v40, 0x3c010204, v40
	v_and_b32_e32 v42, 63, v0
	v_lshlrev_b32_e32 v41, 14, v42
	s_mov_b32 s15, s12
	s_lshl_b32 s15, s15, 2
	s_add_u32 s8, s8, s15
	s_addc_u32 s9, s9, 0
	s_add_u32 s15, s29, 24
	v_cmp_gt_u32_e32 vcc, s15, v42
	s_and_saveexec_b64 s[38:39], vcc
	global_store_dword v41, v40, s[8:9]
	s_mov_b64 exec, s[38:39]
	s_lshl_b32 s15, s14, 12
	v_add_u32_e32 v41, s15, v34
	s_barrier
	ds_write_b128 v41, v[2:5]
	ds_write_b128 v41, v[6:9] offset:1024
	ds_write_b128 v41, v[10:13] offset:2048
	ds_write_b128 v41, v[14:17] offset:3072
	s_waitcnt lgkmcnt(0)
	s_barrier
	s_movk_i32 s15, 0x100
	v_cmp_gt_u32_e32 vcc, s15, v0
	s_and_saveexec_b64 s[38:39], vcc
	s_cbranch_execz .Lk1_end
	v_lshlrev_b32_e32 v16, 4, v0
	ds_read_b128 v[2:5], v16
	ds_read_b128 v[18:21], v16 offset:4096
	ds_read_b128 v[22:25], v16 offset:8192
	ds_read_b128 v[26:29], v16 offset:12288
	ds_read_b128 v[30:33], v16 offset:16384
	ds_read_b128 v[34:37], v16 offset:20480
	ds_read_b128 v[38:41], v16 offset:24576
	ds_read_b128 v[42:45], v16 offset:28672
	s_waitcnt lgkmcnt(6)
	v_pk_add_f32 v[2:3], v[2:3], v[18:19]
	v_pk_add_f32 v[4:5], v[4:5], v[20:21]
	s_waitcnt lgkmcnt(5)
	v_pk_add_f32 v[2:3], v[2:3], v[22:23]
	v_pk_add_f32 v[4:5], v[4:5], v[24:25]
	s_waitcnt lgkmcnt(4)
	v_pk_add_f32 v[2:3], v[2:3], v[26:27]
	v_pk_add_f32 v[4:5], v[4:5], v[28:29]
	s_waitcnt lgkmcnt(3)
	v_pk_add_f32 v[2:3], v[2:3], v[30:31]
	v_pk_add_f32 v[4:5], v[4:5], v[32:33]
	s_waitcnt lgkmcnt(2)
	v_pk_add_f32 v[2:3], v[2:3], v[34:35]
	v_pk_add_f32 v[4:5], v[4:5], v[36:37]
	s_waitcnt lgkmcnt(1)
	v_pk_add_f32 v[2:3], v[2:3], v[38:39]
	v_pk_add_f32 v[4:5], v[4:5], v[40:41]
	s_waitcnt lgkmcnt(0)
	v_pk_add_f32 v[2:3], v[2:3], v[42:43]
	v_pk_add_f32 v[4:5], v[4:5], v[44:45]
	s_lshl_b32 s15, s2, 12
	s_add_u32 s10, s10, s15
	s_addc_u32 s11, s11, 0
	global_store_dwordx4 v16, v[2:5], s[10:11]
